# speedup vs baseline: 1.0300x; 1.0200x over previous
.Lpro_zero:
	v_add_u32_e32 v78, 64, v78
	v_cmp_lt_u32_e32 vcc, s3, v78
	ds_write_b128 v79, v[74:77]
	s_or_b64 s[0:1], vcc, s[0:1]
	v_add_u32_e32 v79, 0x400, v79
	s_andn2_b64 exec, exec, s[0:1]
	s_cbranch_execnz .Lpro_zero
	s_or_b64 exec, exec, s[0:1]
	v_mov_b32_e32 v3, 0x3c00
	v_cndmask_b32_e64 v3, 0, v3, s[4:5]
	v_pack_b32_f16 v96, v3, 0
	v_mov_b32_e32 v97, 0
	v_mov_b32_e32 v98, 0
	v_mov_b32_e32 v99, 0
	v_mov_b32_e32 v77, 0
	v_mov_b32_e32 v78, 0
	v_mov_b32_e32 v79, 0
	v_mov_b32_e32 v53, 0
	v_mov_b32_e32 v54, 0
	v_mov_b32_e32 v55, 0
	s_waitcnt vmcnt(43)
	v_and_b32_e32 v76, 0xffff, v72
	v_and_b32_e32 v52, 0xffff, v73
	s_nop 1
	v_mfma_f32_32x32x16_f16 v[2:17], v[76:79], v[96:99], 0
	v_mfma_f32_32x32x16_f16 v[18:33], v[52:55], v[96:99], 0
	s_waitcnt vmcnt(31)
	v_mfma_f32_32x32x16_f16 v[2:17], v[220:223], v[56:59], v[2:17]
	v_mfma_f32_32x32x16_f16 v[18:33], v[224:227], v[56:59], v[18:33]
	v_mfma_f32_32x32x16_f16 v[2:17], v[228:231], v[60:63], v[2:17]
	v_mfma_f32_32x32x16_f16 v[18:33], v[232:235], v[60:63], v[18:33]
	v_mfma_f32_32x32x16_f16 v[2:17], v[236:239], v[64:67], v[2:17]
	v_mfma_f32_32x32x16_f16 v[18:33], v[240:243], v[64:67], v[18:33]
	v_mfma_f32_32x32x16_f16 v[2:17], v[244:247], v[68:71], v[2:17]
	v_mfma_f32_32x32x16_f16 v[18:33], v[248:251], v[68:71], v[18:33]
	v_readfirstlane_b32 s0, v0
	s_mov_b32 s3, 0
	s_nop 11
	v_cvt_pk_f16_f32 v9, v8, v9
	v_cvt_pk_f16_f32 v8, v6, v7
	v_cvt_pk_f16_f32 v7, v4, v5
	v_cvt_pk_f16_f32 v6, v2, v3
	v_cvt_pk_f16_f32 v5, v24, v25
	v_cvt_pk_f16_f32 v4, v22, v23
	v_cvt_pk_f16_f32 v3, v20, v21
	v_cvt_pk_f16_f32 v2, v18, v19
	v_cvt_pk_f16_f32 v17, v16, v17
	v_cvt_pk_f16_f32 v16, v14, v15
	v_cvt_pk_f16_f32 v15, v12, v13
	v_cvt_pk_f16_f32 v14, v10, v11
	v_cvt_pk_f16_f32 v11, v32, v33
	v_cvt_pk_f16_f32 v10, v30, v31
	ds_write_b128 v211, v[6:9] offset:13632
	ds_write_b128 v211, v[2:5] offset:15680
	ds_write_b128 v211, v[14:17] offset:14656
	v_cvt_pk_f16_f32 v9, v28, v29
	v_cvt_pk_f16_f32 v8, v26, v27
	ds_write_b128 v211, v[8:11] offset:16704
	s_cmpk_lt_i32 s0, 0x100
	s_cselect_b32 s44, 0, 1
.LBB0_20:
	v_mov_b32_e32 v81, 0
	v_lshlrev_b32_e32 v4, 3, v0
	v_lshrrev_b32_e32 v2, 2, v0
	v_lshlrev_b32_e32 v3, 1, v0
	v_bfe_i32 v5, v0, 0, 1
	v_lshrrev_b32_e32 v0, 5, v0
	v_and_b32_e32 v5, 0x120, v5
	v_and_b32_e32 v221, 12, v0
	v_add_u16_e32 v0, v214, v212
	v_add_u32_e32 v5, v50, v5
	v_mul_u32_u24_e32 v1, 0x2800, v1
	v_lshrrev_b16_e32 v0, 1, v0
	v_or_b32_e32 v1, v1, v214
	v_lshl_add_u32 v223, v0, 2, v5
	v_add_lshl_u32 v0, v214, v212, 1
	v_lshlrev_b32_e32 v216, 2, v51
	s_movk_i32 s0, 0x88
	v_add_u32_e32 v222, 0x22a00, v1
	v_add_u32_e32 v1, 64, v0
	v_add_u32_e32 v0, 0xc0, v0
	v_and_or_b32 v2, v2, 3, v216
	v_lshlrev_b32_e32 v6, 4, v212
	v_mad_u32_u24 v8, v212, s0, v50
	v_and_b32_e32 v0, 0x1fc, v0
	s_movk_i32 s0, 0x880
	v_mul_u32_u24_e32 v2, 0x88, v2
	v_and_b32_e32 v3, 32, v3
	v_add_u32_e32 v7, v50, v6
	v_add_u32_e32 v225, v5, v0
	v_mad_u32_u24 v0, v51, s0, v50
	s_movk_i32 s0, 0x240
	v_and_b32_e32 v4, 24, v4
	v_add3_u32 v2, v50, v2, v3
	v_and_b32_e32 v1, 0xfc, v1
	v_add3_u32 v226, v0, v6, s0
	v_add_u32_e32 v228, v7, v214
	v_mbcnt_lo_u32_b32 v0, -1, 0
	v_and_b32_e32 v80, 0xffff, v39
	v_mov_b32_e32 v82, v81
	v_mov_b32_e32 v83, v81
	v_and_b32_e32 v204, 0xffff, v38
	v_mov_b32_e32 v205, v81
	v_mov_b32_e32 v206, v81
	v_mov_b32_e32 v207, v81
	v_lshl_add_u32 v220, v215, 1, v50
	v_add_u32_e32 v224, v5, v1
	s_brev_b32 s33, 61
	s_brev_b32 s34, 60
	s_mov_b32 s35, 0x7fff7fff
	s_mov_b32 s42, 0xa714a714
	v_mov_b32_e32 v227, 0xb7d0b7d0
	s_mov_b32 s43, 0xbc90bc90
	v_add_u32_e32 v229, v8, v214
	v_add_u32_e32 v230, v2, v4
	v_add_u32_e32 v231, 0xf0, v228
	v_add_u32_e32 v232, 0x170, v228
	v_add_u32_e32 v233, 0x1f0, v228
	v_add_u32_e32 v234, 0x70, v228
	v_mbcnt_hi_u32_b32 v235, -1, v0
	v_add_u32_e32 v246, 0x2000, v229
	v_xor_b32_e32 v245, 32, v235
	v_lshlrev_b32_e32 v245, 2, v245
	s_waitcnt vmcnt(28)
	s_branch .LBB0_22

.LBB0_22:
	s_cmp_lt_u32 s3, 2
	s_cselect_b32 s45, 1, 0
	s_xor_b32 s45, s45, s44
	s_cmp_eq_u32 s45, 0
	s_cbranch_scc0 .Lprio_lo
	s_setprio 1
	s_branch .Lprio_done
.Lprio_lo:
	s_setprio 0

.LBB0_25:
	v_mfma_f32_32x32x16_f16 v[48:63], v[80:83], v[96:99], 0
	v_add_u32_e32 v44, s8, v226
	ds_read_b128 v[32:35], v44
	ds_read_b128 v[36:39], v44 offset:4352
	v_mfma_f32_32x32x16_f16 v[64:79], v[204:207], v[96:99], 0
	s_waitcnt lgkmcnt(1)
	v_mfma_f32_32x32x16_f16 v[48:63], v[88:91], v[32:35], v[48:63]
	ds_read_b128 v[40:43], v44 offset:16
	v_mfma_f32_32x32x16_f16 v[64:79], v[84:87], v[32:35], v[64:79]
	s_waitcnt lgkmcnt(1)
	v_mfma_f32_32x32x16_f16 v[48:63], v[100:103], v[36:39], v[48:63]
	ds_read_b128 v[32:35], v44 offset:4368
	v_mfma_f32_32x32x16_f16 v[64:79], v[92:95], v[36:39], v[64:79]
	s_waitcnt lgkmcnt(1)
	v_mfma_f32_32x32x16_f16 v[48:63], v[108:111], v[40:43], v[48:63]
	ds_read_b128 v[36:39], v44 offset:32
	v_mfma_f32_32x32x16_f16 v[64:79], v[104:107], v[40:43], v[64:79]
	s_waitcnt lgkmcnt(1)
	v_mfma_f32_32x32x16_f16 v[48:63], v[116:119], v[32:35], v[48:63]
	ds_read_b128 v[40:43], v44 offset:4384
	v_mfma_f32_32x32x16_f16 v[64:79], v[112:115], v[32:35], v[64:79]
	s_waitcnt lgkmcnt(1)
	v_mfma_f32_32x32x16_f16 v[48:63], v[120:123], v[36:39], v[48:63]
	ds_read_b128 v[32:35], v44 offset:48
	v_mfma_f32_32x32x16_f16 v[64:79], v[128:131], v[36:39], v[64:79]
	s_waitcnt lgkmcnt(1)
	v_mfma_f32_32x32x16_f16 v[48:63], v[152:155], v[40:43], v[48:63]
	ds_read_b128 v[36:39], v44 offset:4400
	v_mfma_f32_32x32x16_f16 v[64:79], v[124:127], v[40:43], v[64:79]
	s_waitcnt lgkmcnt(1)
	v_mfma_f32_32x32x16_f16 v[48:63], v[136:139], v[32:35], v[48:63]
	ds_read_b128 v[40:43], v44 offset:64
	v_mfma_f32_32x32x16_f16 v[64:79], v[132:135], v[32:35], v[64:79]
	s_waitcnt lgkmcnt(1)
	v_mfma_f32_32x32x16_f16 v[48:63], v[144:147], v[36:39], v[48:63]
	ds_read_b128 v[32:35], v44 offset:4416
	v_mfma_f32_32x32x16_f16 v[64:79], v[140:143], v[36:39], v[64:79]
	s_waitcnt lgkmcnt(1)
	v_mfma_f32_32x32x16_f16 v[48:63], v[156:159], v[40:43], v[48:63]
	ds_read_b128 v[36:39], v44 offset:80
	v_mfma_f32_32x32x16_f16 v[64:79], v[148:151], v[40:43], v[64:79]
	s_waitcnt lgkmcnt(1)
	v_mfma_f32_32x32x16_f16 v[48:63], v[164:167], v[32:35], v[48:63]
	ds_read_b128 v[40:43], v44 offset:4432
	v_mfma_f32_32x32x16_f16 v[64:79], v[160:163], v[32:35], v[64:79]
	s_waitcnt lgkmcnt(1)
	v_mfma_f32_32x32x16_f16 v[48:63], v[172:175], v[36:39], v[48:63]
	ds_read_b128 v[32:35], v44 offset:96
	v_mfma_f32_32x32x16_f16 v[64:79], v[168:171], v[36:39], v[64:79]
	s_waitcnt lgkmcnt(1)
	v_mfma_f32_32x32x16_f16 v[48:63], v[180:183], v[40:43], v[48:63]
	ds_read_b128 v[36:39], v44 offset:4448
	v_mfma_f32_32x32x16_f16 v[64:79], v[176:179], v[40:43], v[64:79]
	s_waitcnt lgkmcnt(1)
	v_mfma_f32_32x32x16_f16 v[48:63], v[188:191], v[32:35], v[48:63]
	v_mfma_f32_32x32x16_f16 v[64:79], v[184:187], v[32:35], v[64:79]
	s_waitcnt lgkmcnt(0)
	v_mfma_f32_32x32x16_f16 v[48:63], v[196:199], v[36:39], v[48:63]
	v_mfma_f32_32x32x16_f16 v[64:79], v[192:195], v[36:39], v[64:79]
	s_nop 15
	s_nop 3
	ds_read_b128 v[32:35], v211 offset:13632
	v_cvt_pk_f16_f32 v38, v64, v65
	v_cvt_pk_f16_f32 v39, v66, v67
	v_and_b32 v36, s35, v38
	v_and_b32 v37, s35, v39
	v_pk_fma_f16 v238, v36, s42, v227
	v_pk_fma_f16 v239, v37, s42, v227
	v_pk_fma_f16 v238, v238, v36, s43
	v_pk_fma_f16 v239, v239, v37, s43
	s_nop 10
	ds_read_b128 v[64:67], v211 offset:14656
	v_pk_mul_f16 v238, v238, v36
	v_pk_mul_f16 v239, v239, v37
	v_exp_f16_sdwa v238, v238 dst_sel:WORD_0 dst_unused:UNUSED_PRESERVE src0_sel:WORD_0
	v_exp_f16_sdwa v239, v239 dst_sel:WORD_0 dst_unused:UNUSED_PRESERVE src0_sel:WORD_0
	v_exp_f16_sdwa v238, v238 dst_sel:WORD_1 dst_unused:UNUSED_PRESERVE src0_sel:WORD_1
	v_exp_f16_sdwa v239, v239 dst_sel:WORD_1 dst_unused:UNUSED_PRESERVE src0_sel:WORD_1
	v_pk_add_f16 v40, v38, v36
	v_pk_add_f16 v41, v39, v37
	v_pk_fma_f16 v238, v36, v238, v40 neg_lo:[1,0,0] neg_hi:[1,0,0]
	v_pk_fma_f16 v239, v37, v239, v41 neg_lo:[1,0,0] neg_hi:[1,0,0]
	v_cvt_pk_f16_f32 v38, v68, v69
	v_cvt_pk_f16_f32 v39, v70, v71
	v_and_b32 v36, s35, v38
	v_and_b32 v37, s35, v39
	v_pk_fma_f16 v240, v36, s42, v227
	v_pk_fma_f16 v241, v37, s42, v227
	v_pk_fma_f16 v240, v240, v36, s43
	v_pk_fma_f16 v241, v241, v37, s43
	v_cvt_pk_f16_f32 v243, v72, v73
	v_cvt_pk_f16_f32 v244, v74, v75
	v_and_b32 v209, s35, v243
	v_and_b32 v242, s35, v244
	v_pk_fma_f16 v68, v209, s42, v227
	v_pk_fma_f16 v69, v242, s42, v227
	v_pk_fma_f16 v68, v68, v209, s43
	v_pk_fma_f16 v69, v69, v242, s43
	v_cvt_pk_f16_f32 v74, v76, v77
	v_cvt_pk_f16_f32 v75, v78, v79
	v_and_b32 v72, s35, v74
	v_and_b32 v73, s35, v75
	v_pk_fma_f16 v70, v72, s42, v227
	v_pk_fma_f16 v71, v73, s42, v227
	v_pk_fma_f16 v70, v70, v72, s43
	v_pk_fma_f16 v71, v71, v73, s43
	s_cmp_eq_u32 s8, 0
	v_pk_mul_f16 v240, v240, v36
	v_pk_mul_f16 v241, v241, v37
	v_exp_f16_sdwa v240, v240 dst_sel:WORD_0 dst_unused:UNUSED_PRESERVE src0_sel:WORD_0
	v_exp_f16_sdwa v241, v241 dst_sel:WORD_0 dst_unused:UNUSED_PRESERVE src0_sel:WORD_0
	v_exp_f16_sdwa v240, v240 dst_sel:WORD_1 dst_unused:UNUSED_PRESERVE src0_sel:WORD_1
	v_exp_f16_sdwa v241, v241 dst_sel:WORD_1 dst_unused:UNUSED_PRESERVE src0_sel:WORD_1
	v_pk_add_f16 v40, v38, v36
	v_pk_add_f16 v41, v39, v37
	v_pk_fma_f16 v240, v36, v240, v40 neg_lo:[1,0,0] neg_hi:[1,0,0]
	v_pk_fma_f16 v241, v37, v241, v41 neg_lo:[1,0,0] neg_hi:[1,0,0]
	v_pk_mul_f16 v68, v68, v209
	v_pk_mul_f16 v69, v69, v242
	v_exp_f16_sdwa v68, v68 dst_sel:WORD_0 dst_unused:UNUSED_PRESERVE src0_sel:WORD_0
	v_exp_f16_sdwa v69, v69 dst_sel:WORD_0 dst_unused:UNUSED_PRESERVE src0_sel:WORD_0
	v_exp_f16_sdwa v68, v68 dst_sel:WORD_1 dst_unused:UNUSED_PRESERVE src0_sel:WORD_1
	v_exp_f16_sdwa v69, v69 dst_sel:WORD_1 dst_unused:UNUSED_PRESERVE src0_sel:WORD_1
	v_pk_add_f16 v76, v243, v209
	v_pk_add_f16 v77, v244, v242
	v_pk_fma_f16 v68, v209, v68, v76 neg_lo:[1,0,0] neg_hi:[1,0,0]
	v_pk_fma_f16 v69, v242, v69, v77 neg_lo:[1,0,0] neg_hi:[1,0,0]
	s_waitcnt lgkmcnt(1)
	v_mfma_f32_32x32x16_f16 v[32:47], v[238:241], v[32:35], 0
	v_pk_mul_f16 v70, v70, v72
	v_pk_mul_f16 v71, v71, v73
	v_exp_f16_sdwa v70, v70 dst_sel:WORD_0 dst_unused:UNUSED_PRESERVE src0_sel:WORD_0
	v_exp_f16_sdwa v71, v71 dst_sel:WORD_0 dst_unused:UNUSED_PRESERVE src0_sel:WORD_0
	v_exp_f16_sdwa v70, v70 dst_sel:WORD_1 dst_unused:UNUSED_PRESERVE src0_sel:WORD_1
	v_exp_f16_sdwa v71, v71 dst_sel:WORD_1 dst_unused:UNUSED_PRESERVE src0_sel:WORD_1
	v_pk_add_f16 v76, v74, v72
	v_pk_add_f16 v77, v75, v73
	v_pk_fma_f16 v70, v72, v70, v76 neg_lo:[1,0,0] neg_hi:[1,0,0]
	v_pk_fma_f16 v71, v73, v71, v77 neg_lo:[1,0,0] neg_hi:[1,0,0]
	s_waitcnt lgkmcnt(0)
	v_mfma_f32_32x32x16_f16 v[32:47], v[68:71], v[64:67], v[32:47]
	v_cvt_pk_f16_f32 v74, v48, v49
	v_cvt_pk_f16_f32 v75, v50, v51
	v_and_b32 v72, s35, v74
	v_and_b32 v73, s35, v75
	v_pk_fma_f16 v64, v72, s42, v227
	v_pk_fma_f16 v65, v73, s42, v227
	v_pk_fma_f16 v64, v64, v72, s43
	v_pk_fma_f16 v65, v65, v73, s43
	ds_read_b128 v[48:51], v211 offset:15680
	v_cvt_pk_f16_f32 v78, v52, v53
	v_cvt_pk_f16_f32 v79, v54, v55
	v_and_b32 v76, s35, v78
	v_and_b32 v77, s35, v79
	v_pk_fma_f16 v66, v76, s42, v227
	v_pk_fma_f16 v67, v77, s42, v227
	v_pk_fma_f16 v66, v66, v76, s43
	v_pk_fma_f16 v67, v67, v77, s43
	ds_read_b128 v[52:55], v211 offset:16704
	v_pk_mul_f16 v64, v64, v72
	v_pk_mul_f16 v65, v65, v73
	v_exp_f16_sdwa v64, v64 dst_sel:WORD_0 dst_unused:UNUSED_PRESERVE src0_sel:WORD_0
	v_exp_f16_sdwa v65, v65 dst_sel:WORD_0 dst_unused:UNUSED_PRESERVE src0_sel:WORD_0
	v_exp_f16_sdwa v64, v64 dst_sel:WORD_1 dst_unused:UNUSED_PRESERVE src0_sel:WORD_1
	v_exp_f16_sdwa v65, v65 dst_sel:WORD_1 dst_unused:UNUSED_PRESERVE src0_sel:WORD_1
	v_pk_add_f16 v209, v74, v72
	v_pk_add_f16 v242, v75, v73
	v_pk_fma_f16 v64, v72, v64, v209 neg_lo:[1,0,0] neg_hi:[1,0,0]
	v_pk_fma_f16 v65, v73, v65, v242 neg_lo:[1,0,0] neg_hi:[1,0,0]
	v_pk_mul_f16 v66, v66, v76
	v_pk_mul_f16 v67, v67, v77
	v_exp_f16_sdwa v66, v66 dst_sel:WORD_0 dst_unused:UNUSED_PRESERVE src0_sel:WORD_0
	v_exp_f16_sdwa v67, v67 dst_sel:WORD_0 dst_unused:UNUSED_PRESERVE src0_sel:WORD_0
	v_exp_f16_sdwa v66, v66 dst_sel:WORD_1 dst_unused:UNUSED_PRESERVE src0_sel:WORD_1
	v_exp_f16_sdwa v67, v67 dst_sel:WORD_1 dst_unused:UNUSED_PRESERVE src0_sel:WORD_1
	v_pk_add_f16 v72, v78, v76
	v_pk_add_f16 v73, v79, v77
	v_pk_fma_f16 v66, v76, v66, v72 neg_lo:[1,0,0] neg_hi:[1,0,0]
	v_pk_fma_f16 v67, v77, v67, v73 neg_lo:[1,0,0] neg_hi:[1,0,0]
	s_waitcnt lgkmcnt(1)
	v_mfma_f32_32x32x16_f16 v[32:47], v[64:67], v[48:51], v[32:47]
	v_cvt_pk_f16_f32 v74, v56, v57
	v_cvt_pk_f16_f32 v75, v58, v59
	v_and_b32 v72, s35, v74
	v_and_b32 v73, s35, v75
	v_pk_fma_f16 v48, v72, s42, v227
	v_pk_fma_f16 v49, v73, s42, v227
	v_pk_fma_f16 v48, v48, v72, s43
	v_pk_fma_f16 v49, v49, v73, s43
	v_cvt_pk_f16_f32 v58, v60, v61
	v_cvt_pk_f16_f32 v59, v62, v63
	v_and_b32 v56, s35, v58
	v_and_b32 v57, s35, v59
	v_pk_fma_f16 v50, v56, s42, v227
	v_pk_fma_f16 v51, v57, s42, v227
	v_pk_fma_f16 v50, v50, v56, s43
	v_pk_fma_f16 v51, v51, v57, s43
	v_pk_mul_f16 v48, v48, v72
	v_pk_mul_f16 v49, v49, v73
	v_exp_f16_sdwa v48, v48 dst_sel:WORD_0 dst_unused:UNUSED_PRESERVE src0_sel:WORD_0
	v_exp_f16_sdwa v49, v49 dst_sel:WORD_0 dst_unused:UNUSED_PRESERVE src0_sel:WORD_0
	v_exp_f16_sdwa v48, v48 dst_sel:WORD_1 dst_unused:UNUSED_PRESERVE src0_sel:WORD_1
	v_exp_f16_sdwa v49, v49 dst_sel:WORD_1 dst_unused:UNUSED_PRESERVE src0_sel:WORD_1
	v_pk_add_f16 v62, v74, v72
	v_pk_add_f16 v63, v75, v73
	v_pk_fma_f16 v48, v72, v48, v62 neg_lo:[1,0,0] neg_hi:[1,0,0]
	v_pk_fma_f16 v49, v73, v49, v63 neg_lo:[1,0,0] neg_hi:[1,0,0]
	v_pk_mul_f16 v50, v50, v56
	v_pk_mul_f16 v51, v51, v57
	v_exp_f16_sdwa v50, v50 dst_sel:WORD_0 dst_unused:UNUSED_PRESERVE src0_sel:WORD_0
	v_exp_f16_sdwa v51, v51 dst_sel:WORD_0 dst_unused:UNUSED_PRESERVE src0_sel:WORD_0
	v_exp_f16_sdwa v50, v50 dst_sel:WORD_1 dst_unused:UNUSED_PRESERVE src0_sel:WORD_1
	v_exp_f16_sdwa v51, v51 dst_sel:WORD_1 dst_unused:UNUSED_PRESERVE src0_sel:WORD_1
	v_pk_add_f16 v62, v58, v56
	v_pk_add_f16 v63, v59, v57
	v_pk_fma_f16 v50, v56, v50, v62 neg_lo:[1,0,0] neg_hi:[1,0,0]
	v_pk_fma_f16 v51, v57, v51, v63 neg_lo:[1,0,0] neg_hi:[1,0,0]
	ds_write2_b64 v246, v[238:239], v[240:241] offset0:136 offset1:138
	ds_write2_b64 v246, v[64:65], v[66:67] offset0:144 offset1:146
	ds_write2_b64 v246, v[68:69], v[70:71] offset0:140 offset1:142
	ds_write2_b64 v246, v[48:49], v[50:51] offset0:148 offset1:150
	s_waitcnt lgkmcnt(4)
	v_mfma_f32_32x32x16_f16 v[32:47], v[48:51], v[52:55], v[32:47]
	s_nop 11
	v_max_f32_e32 v52, v33, v33
	v_max_f32_e32 v53, v32, v32
	v_max_f32_e32 v52, v53, v52
	v_max3_f32 v52, v52, v34, v35
	v_max3_f32 v52, v52, v36, v37
	v_max3_f32 v52, v52, v38, v39
	v_max3_f32 v52, v52, v40, v41
	v_max3_f32 v52, v52, v42, v43
	v_max3_f32 v52, v52, v44, v45
	v_max3_f32 v52, v52, v46, v47
	ds_bpermute_b32 v53, v245, v52
	s_waitcnt lgkmcnt(0)
	v_max_f32_e32 v48, v53, v53
	v_max_f32_e32 v48, v52, v48
	s_cbranch_scc1 .LBB0_23
	v_add_f32_e32 v49, 0x41000000, v237
	v_cmp_gt_f32_e32 vcc, v48, v49
	s_cbranch_vccz .LBB0_24
	v_max_f32_e32 v48, v48, v48
	v_max_f32_e32 v49, v237, v237
	v_max_f32_e32 v49, v49, v48
	v_sub_f32_e32 v48, v237, v49
	v_exp_f32_e32 v48, v48
	v_mov_b32_e32 v237, v49
	v_pk_mul_f32 v[14:15], v[48:49], v[14:15] op_sel_hi:[0,1]
	v_pk_mul_f32 v[12:13], v[48:49], v[12:13] op_sel_hi:[0,1]
	v_pk_mul_f32 v[10:11], v[48:49], v[10:11] op_sel_hi:[0,1]
	v_pk_mul_f32 v[8:9], v[48:49], v[8:9] op_sel_hi:[0,1]
	v_pk_mul_f32 v[6:7], v[48:49], v[6:7] op_sel_hi:[0,1]
	v_pk_mul_f32 v[4:5], v[48:49], v[4:5] op_sel_hi:[0,1]
	v_pk_mul_f32 v[2:3], v[48:49], v[2:3] op_sel_hi:[0,1]
	v_pk_mul_f32 v[0:1], v[48:49], v[0:1] op_sel_hi:[0,1]
	v_pk_mul_f32 v[30:31], v[48:49], v[30:31] op_sel_hi:[0,1]
	v_pk_mul_f32 v[28:29], v[48:49], v[28:29] op_sel_hi:[0,1]
	v_pk_mul_f32 v[26:27], v[48:49], v[26:27] op_sel_hi:[0,1]
	v_pk_mul_f32 v[24:25], v[48:49], v[24:25] op_sel_hi:[0,1]
	v_pk_mul_f32 v[22:23], v[48:49], v[22:23] op_sel_hi:[0,1]
	v_pk_mul_f32 v[20:21], v[48:49], v[20:21] op_sel_hi:[0,1]
	v_pk_mul_f32 v[18:19], v[48:49], v[18:19] op_sel_hi:[0,1]
	v_pk_mul_f32 v[16:17], v[48:49], v[16:17] op_sel_hi:[0,1]
	v_mul_f32_e32 v236, v236, v48
	s_branch .LBB0_24
.LBB0_28:
	ds_bpermute_b32 v32, v245, v236
	s_mul_i32 s8, s3, 5
	s_add_i32 s0, s8, 5
	v_cmp_le_u32_e32 vcc, s8, v212
	v_cmp_gt_u32_e64 s[0:1], s0, v212
	s_and_b64 s[10:11], vcc, s[0:1]
	s_and_saveexec_b64 s[0:1], s[10:11]
	s_cbranch_execz .LBB0_21
	s_waitcnt lgkmcnt(0)
	v_add_f32_e32 v32, v236, v32
	v_div_scale_f32 v33, s[10:11], v32, v32, 0.5
	v_rcp_f32_e32 v34, v33
	v_div_scale_f32 v35, vcc, 0.5, v32, 0.5
	v_fma_f32 v36, -v33, v34, 1.0
	v_fmac_f32_e32 v34, v36, v34
	v_mul_f32_e32 v36, v35, v34
	v_fma_f32 v37, -v33, v36, v35
	v_fmac_f32_e32 v36, v37, v34
	v_fma_f32 v33, -v33, v36, v35
	v_div_fmas_f32 v33, v33, v34, v36
	v_div_fixup_f32 v32, v33, v32, 0.5
	v_add_u32_e32 v33, s3, v221
	v_subrev_u32_e32 v34, s8, v212
	v_mad_u64_u32 v[34:35], s[8:9], v33, 5, v[34:35]
	v_lshl_add_u32 v33, v34, 7, v222
	v_pk_mul_f32 v[0:1], v[32:33], v[0:1] op_sel_hi:[0,1]
	v_pk_mul_f32 v[2:3], v[32:33], v[2:3] op_sel_hi:[0,1]
	v_cvt_pk_f16_f32 v3, v2, v3
	v_cvt_pk_f16_f32 v2, v0, v1
	v_pk_mul_f32 v[0:1], v[32:33], v[16:17] op_sel_hi:[0,1]
	v_pk_mul_f32 v[16:17], v[32:33], v[18:19] op_sel_hi:[0,1]
	v_cvt_pk_f16_f32 v17, v16, v17
	v_cvt_pk_f16_f32 v16, v0, v1
	v_pk_mul_f32 v[0:1], v[32:33], v[4:5] op_sel_hi:[0,1]
	v_pk_mul_f32 v[4:5], v[32:33], v[6:7] op_sel_hi:[0,1]
	v_cvt_pk_f16_f32 v5, v4, v5
	v_cvt_pk_f16_f32 v4, v0, v1
	ds_write2_b64 v33, v[2:3], v[4:5] offset1:2
	v_pk_mul_f32 v[0:1], v[32:33], v[20:21] op_sel_hi:[0,1]
	v_pk_mul_f32 v[2:3], v[32:33], v[22:23] op_sel_hi:[0,1]
	v_cvt_pk_f16_f32 v3, v2, v3
	v_cvt_pk_f16_f32 v2, v0, v1
	ds_write2_b64 v33, v[16:17], v[2:3] offset0:8 offset1:10
	v_pk_mul_f32 v[0:1], v[32:33], v[8:9] op_sel_hi:[0,1]
	v_pk_mul_f32 v[2:3], v[32:33], v[10:11] op_sel_hi:[0,1]
	v_cvt_pk_f16_f32 v3, v2, v3
	v_cvt_pk_f16_f32 v2, v0, v1
	v_pk_mul_f32 v[0:1], v[32:33], v[24:25] op_sel_hi:[0,1]
	v_pk_mul_f32 v[4:5], v[32:33], v[26:27] op_sel_hi:[0,1]
	v_cvt_pk_f16_f32 v5, v4, v5
	v_cvt_pk_f16_f32 v4, v0, v1
	v_pk_mul_f32 v[0:1], v[32:33], v[12:13] op_sel_hi:[0,1]
	v_pk_mul_f32 v[6:7], v[32:33], v[14:15] op_sel_hi:[0,1]
	v_cvt_pk_f16_f32 v7, v6, v7
	v_cvt_pk_f16_f32 v6, v0, v1
	ds_write2_b64 v33, v[2:3], v[6:7] offset0:4 offset1:6
	v_pk_mul_f32 v[0:1], v[32:33], v[28:29] op_sel_hi:[0,1]
	v_pk_mul_f32 v[2:3], v[32:33], v[30:31] op_sel_hi:[0,1]
	v_cvt_pk_f16_f32 v3, v2, v3
	v_cvt_pk_f16_f32 v2, v0, v1
	ds_write2_b64 v33, v[4:5], v[2:3] offset0:12 offset1:14
	s_branch .LBB0_21
.LBB0_30:
	v_mov_b32_e32 v209, v245
	v_readfirstlane_b32 s0, v213
	s_cmp_lt_i32 s0, 3
	s_waitcnt lgkmcnt(0)
	s_cbranch_scc0 .Lhead_idle
	v_mov_b32_e32 v83, 0
	v_mov_b32_e32 v211, v83
	v_lshl_add_u64 v[156:157], s[36:37], 0, v[210:211]
	s_movk_i32 s0, 0x3000
	v_add_co_u32_e32 v68, vcc, s0, v156
	s_movk_i32 s0, 0x2000
	s_nop 0
	v_addc_co_u32_e32 v69, vcc, 0, v157, vcc
	global_load_dwordx4 v[0:3], v[68:69], off offset:-4096
	v_add_co_u32_e32 v70, vcc, s0, v156
	s_movk_i32 s0, 0x1000
	s_nop 0
	v_addc_co_u32_e32 v71, vcc, 0, v157, vcc
	global_load_dwordx4 v[16:19], v[70:71], off offset:1024
	global_load_dwordx4 v[56:59], v210, s[36:37]
	global_load_dwordx4 v[52:55], v210, s[36:37] offset:1024
	global_load_dwordx4 v[48:51], v210, s[36:37] offset:2048
	global_load_dwordx4 v[44:47], v210, s[36:37] offset:3072
	v_add_co_u32_e32 v20, vcc, s0, v156
	s_movk_i32 s0, 0x50
	s_nop 0
	v_addc_co_u32_e32 v21, vcc, 0, v157, vcc
	global_load_dwordx4 v[40:43], v[20:21], off
	global_load_dwordx4 v[36:39], v[20:21], off offset:1024
	global_load_dwordx4 v[32:35], v[20:21], off offset:2048
	global_load_dwordx4 v[60:63], v[68:69], off
	global_load_dwordx4 v[72:75], v[20:21], off offset:3072
	global_load_dwordx4 v[76:79], v[70:71], off offset:2048
	s_barrier
	v_lshl_or_b32 v20, v213, 5, v212
	v_mov_b32_e32 v21, 0x4f
	v_cmp_gt_u32_e64 s[0:1], s0, v20
	s_lshl_b32 s2, s2, 2
	s_movk_i32 s3, 0x4000
	v_cndmask_b32_e64 v100, v21, v20, s[0:1]
	v_lshl_or_b32 v64, v100, 7, v208
	v_add_u32_e32 v127, 0x22a00, v64
	ds_read_b128 v[64:67], v127
	ds_read_b128 v[84:87], v127 offset:32
	s_mov_b32 s9, 0x66666667
	v_add_co_u32_e32 v108, vcc, s3, v156
	s_movk_i32 s10, 0x5000
	s_nop 0
	v_addc_co_u32_e32 v109, vcc, 0, v157, vcc
	v_add_co_u32_e32 v152, vcc, s10, v156
	v_lshlrev_b32_e32 v82, 1, v214
	s_nop 0
	v_addc_co_u32_e32 v153, vcc, 0, v157, vcc
	v_mov_b32_e32 v126, 0x3727c5ac
	s_mov_b32 s8, 0xf800000
	v_mov_b32_e32 v208, 0x260
	v_mov_b32_e32 v80, s26
	v_mov_b32_e32 v81, s27
	s_and_b64 s[0:1], s[4:5], s[0:1]
	s_waitcnt vmcnt(10)
	v_mfma_f32_32x32x16_f16 v[16:31], v[16:19], v[96:99], 0
	v_mfma_f32_32x32x16_f16 v[0:15], v[0:3], v[96:99], 0
	s_waitcnt vmcnt(9) lgkmcnt(1)
	v_mfma_f32_32x32x16_f16 v[0:15], v[56:59], v[64:67], v[0:15]
	s_waitcnt vmcnt(8)
	v_mfma_f32_32x32x16_f16 v[16:31], v[52:55], v[64:67], v[16:31]
	v_mul_lo_u16_e32 v52, 0xcd, v100
	v_lshrrev_b16_e32 v52, 10, v52
	v_lshlrev_b32_e32 v102, 10, v52
	v_lshrrev_b32_e32 v101, 2, v52
	v_sub_u32_e32 v103, s2, v52
	s_waitcnt vmcnt(7) lgkmcnt(0)
	v_mfma_f32_32x32x16_f16 v[0:15], v[48:51], v[84:87], v[0:15]
	ds_read_b128 v[48:51], v127 offset:64
	ds_read_b128 v[88:91], v127 offset:96
	s_waitcnt vmcnt(6)
	v_mfma_f32_32x32x16_f16 v[16:31], v[44:47], v[84:87], v[16:31]
	global_load_dwordx4 v[84:87], v[108:109], off offset:2048
	global_load_dwordx4 v[92:95], v[108:109], off offset:3072
	global_load_dwordx4 v[120:123], v[70:71], off offset:3072
	global_load_dwordx4 v[52:55], v[68:69], off offset:1024
	global_load_dwordx4 v[56:59], v[68:69], off offset:2048
	global_load_dwordx4 v[44:47], v[68:69], off offset:3072
	global_load_dwordx4 v[64:67], v[152:153], off offset:-4096
	s_waitcnt vmcnt(12) lgkmcnt(1)
	v_mfma_f32_32x32x16_f16 v[0:15], v[40:43], v[48:51], v[0:15]
	v_and_b32_e32 v40, 0xc00, v102
	v_add3_u32 v40, v103, v101, v40
	v_mad_u64_u32 v[158:159], s[2:3], v40, 5, v[100:101]
	v_mul_hi_i32 v42, v158, s9
	v_lshlrev_b32_e32 v40, 6, v158
	v_ashrrev_i32_e32 v41, 31, v40
	s_waitcnt vmcnt(11)
	v_mfma_f32_32x32x16_f16 v[16:31], v[36:39], v[48:51], v[16:31]
	v_lshrrev_b32_e32 v38, 31, v42
	v_ashrrev_i32_e32 v39, 1, v42
	v_add_u32_e32 v159, v39, v38
	v_lshlrev_b32_e32 v68, 6, v159
	v_ashrrev_i32_e32 v69, 31, v68
	v_lshl_add_u64 v[48:49], v[68:69], 2, s[24:25]
	v_lshl_add_u64 v[36:37], v[40:41], 1, s[6:7]
	s_waitcnt vmcnt(10) lgkmcnt(0)
	v_mfma_f32_32x32x16_f16 v[0:15], v[32:35], v[88:91], v[0:15]
	v_lshl_add_u64 v[70:71], v[36:37], 0, v[82:83]
	v_lshlrev_b32_e32 v82, 2, v216
	v_lshl_add_u64 v[116:117], v[48:49], 0, v[82:83]
	global_load_dwordx4 v[32:35], v82, s[28:29]
	global_load_dwordx4 v[36:39], v82, s[28:29] offset:32
	global_load_dwordx4 v[40:43], v82, s[28:29] offset:64
	global_load_dwordx4 v[128:131], v82, s[28:29] offset:96
	v_add_u32_e32 v68, 0x40000, v68
	s_mov_b32 s6, 0xd000
	s_mov_b32 s7, 0xc000
	s_waitcnt vmcnt(12)
	v_mfma_f32_32x32x16_f16 v[16:31], v[72:75], v[88:91], v[16:31]
	s_nop 11
	v_add_f32_e32 v69, v0, v16
	v_add_f32_e32 v90, v1, v17
	v_add_f32_e32 v69, 0, v69
	v_add_f32_e32 v91, v2, v18
	v_add_f32_e32 v69, v90, v69
	v_add_f32_e32 v100, v3, v19
	v_add_f32_e32 v69, v91, v69
	v_add_f32_e32 v101, v4, v20
	v_add_f32_e32 v69, v100, v69
	v_add_f32_e32 v102, v5, v21
	v_add_f32_e32 v69, v101, v69
	v_pk_add_f32 v[48:49], v[6:7], v[22:23]
	v_add_f32_e32 v69, v102, v69
	v_add_f32_e32 v48, v48, v69
	v_pk_add_f32 v[50:51], v[8:9], v[24:25]
	v_add_f32_e32 v48, v49, v48
	v_add_f32_e32 v48, v50, v48
	v_pk_add_f32 v[72:73], v[10:11], v[26:27]
	v_add_f32_e32 v48, v51, v48
	v_add_f32_e32 v48, v72, v48
	v_pk_add_f32 v[74:75], v[12:13], v[28:29]
	v_add_f32_e32 v48, v73, v48
	v_add_f32_e32 v48, v74, v48
	v_pk_add_f32 v[88:89], v[14:15], v[30:31]
	v_add_f32_e32 v48, v75, v48
	v_add_f32_e32 v48, v88, v48
	v_add_f32_e32 v69, v89, v48
	ds_bpermute_b32 v72, v209, v69
	global_load_dwordx4 v[48:51], v[116:117], off
	global_load_dwordx4 v[88:91], v[116:117], off offset:32
	global_load_dwordx4 v[132:135], v[116:117], off offset:64
	global_load_dwordx4 v[136:139], v[116:117], off offset:96
	global_load_dwordx4 v[104:107], v[70:71], off
	global_load_dwordx4 v[100:103], v[70:71], off offset:32
	global_load_dwordx4 v[140:143], v82, s[28:29] offset:128
	global_load_dwordx4 v[144:147], v82, s[28:29] offset:160
	global_load_dwordx4 v[148:151], v[116:117], off offset:128
	global_load_dwordx4 v[160:163], v82, s[28:29] offset:192
	global_load_dwordx4 v[164:167], v[116:117], off offset:160
	global_load_dwordx4 v[168:171], v[116:117], off offset:192
	global_load_dwordx4 v[172:175], v[108:109], off offset:1024
	s_waitcnt lgkmcnt(0)
	v_add_f32_e32 v69, v69, v72
	v_mul_f32_e32 v72, 0x3c800000, v69
	v_pk_add_f32 v[124:125], v[30:31], v[72:73] op_sel_hi:[1,0] neg_lo:[0,1] neg_hi:[0,1]
	v_pk_add_f32 v[154:155], v[14:15], v[72:73] op_sel_hi:[1,0] neg_lo:[0,1] neg_hi:[0,1]
	v_pk_add_f32 v[184:185], v[28:29], v[72:73] op_sel_hi:[1,0] neg_lo:[0,1] neg_hi:[0,1]
	v_pk_add_f32 v[186:187], v[12:13], v[72:73] op_sel_hi:[1,0] neg_lo:[0,1] neg_hi:[0,1]
	v_pk_add_f32 v[188:189], v[26:27], v[72:73] op_sel_hi:[1,0] neg_lo:[0,1] neg_hi:[0,1]
	v_pk_add_f32 v[190:191], v[10:11], v[72:73] op_sel_hi:[1,0] neg_lo:[0,1] neg_hi:[0,1]
	v_pk_add_f32 v[192:193], v[24:25], v[72:73] op_sel_hi:[1,0] neg_lo:[0,1] neg_hi:[0,1]
	v_pk_add_f32 v[194:195], v[8:9], v[72:73] op_sel_hi:[1,0] neg_lo:[0,1] neg_hi:[0,1]
	v_pk_add_f32 v[196:197], v[22:23], v[72:73] op_sel_hi:[1,0] neg_lo:[0,1] neg_hi:[0,1]
	v_pk_add_f32 v[74:75], v[6:7], v[72:73] op_sel_hi:[1,0] neg_lo:[0,1] neg_hi:[0,1]
	v_pk_add_f32 v[198:199], v[20:21], v[72:73] op_sel_hi:[1,0] neg_lo:[0,1] neg_hi:[0,1]
	v_pk_add_f32 v[118:119], v[4:5], v[72:73] op_sel_hi:[1,0] neg_lo:[0,1] neg_hi:[0,1]
	v_pk_add_f32 v[200:201], v[18:19], v[72:73] op_sel_hi:[1,0] neg_lo:[0,1] neg_hi:[0,1]
	v_pk_add_f32 v[202:203], v[2:3], v[72:73] op_sel_hi:[1,0] neg_lo:[0,1] neg_hi:[0,1]
	v_pk_add_f32 v[204:205], v[16:17], v[72:73] op_sel_hi:[1,0] neg_lo:[0,1] neg_hi:[0,1]
	v_pk_add_f32 v[72:73], v[0:1], v[72:73] op_sel_hi:[1,0] neg_lo:[0,1] neg_hi:[0,1]
	global_load_dwordx4 v[112:115], v[70:71], off offset:64
	global_load_dwordx4 v[108:111], v[70:71], off offset:96
	global_load_dwordx4 v[176:179], v82, s[28:29] offset:224
	global_load_dwordx4 v[180:183], v[116:117], off offset:224
	v_fma_f32 v0, v72, v72, 0
	v_fmac_f32_e32 v0, v204, v204
	v_fmac_f32_e32 v0, v73, v73
	v_fmac_f32_e32 v0, v205, v205
	v_fmac_f32_e32 v0, v202, v202
	v_fmac_f32_e32 v0, v200, v200
	v_fmac_f32_e32 v0, v203, v203
	v_fmac_f32_e32 v0, v201, v201
	v_fmac_f32_e32 v0, v118, v118
	v_fmac_f32_e32 v0, v198, v198
	v_fmac_f32_e32 v0, v119, v119
	v_fmac_f32_e32 v0, v199, v199
	v_fmac_f32_e32 v0, v74, v74
	v_fmac_f32_e32 v0, v196, v196
	v_fmac_f32_e32 v0, v75, v75
	v_fmac_f32_e32 v0, v197, v197
	v_fmac_f32_e32 v0, v194, v194
	v_fmac_f32_e32 v0, v192, v192
	v_fmac_f32_e32 v0, v195, v195
	v_fmac_f32_e32 v0, v193, v193
	v_fmac_f32_e32 v0, v190, v190
	v_fmac_f32_e32 v0, v188, v188
	v_fmac_f32_e32 v0, v191, v191
	v_fmac_f32_e32 v0, v189, v189
	v_fmac_f32_e32 v0, v186, v186
	v_fmac_f32_e32 v0, v184, v184
	v_fmac_f32_e32 v0, v187, v187
	v_fmac_f32_e32 v0, v185, v185
	v_fmac_f32_e32 v0, v154, v154
	v_fmac_f32_e32 v0, v124, v124
	v_fmac_f32_e32 v0, v155, v155
	v_fmac_f32_e32 v0, v125, v125
	ds_bpermute_b32 v1, v209, v0
	s_waitcnt lgkmcnt(0)
	v_add_f32_e32 v0, v0, v1
	v_fmamk_f32 v0, v0, 0x3c800000, v126
	v_mul_f32_e32 v1, 0x4f800000, v0
	v_cmp_gt_f32_e32 vcc, s8, v0
	s_nop 1
	v_cndmask_b32_e32 v0, v0, v1, vcc
	v_sqrt_f32_e32 v1, v0
	s_nop 0
	v_add_u32_e32 v2, -1, v1
	v_fma_f32 v3, -v2, v1, v0
	v_cmp_ge_f32_e64 s[2:3], 0, v3
	v_add_u32_e32 v3, 1, v1
	s_nop 0
	v_cndmask_b32_e64 v2, v1, v2, s[2:3]
	v_fma_f32 v1, -v3, v1, v0
	v_cmp_lt_f32_e64 s[2:3], 0, v1
	s_nop 1
	v_cndmask_b32_e64 v1, v2, v3, s[2:3]
	v_mul_f32_e32 v2, 0x37800000, v1
	v_cndmask_b32_e32 v1, v1, v2, vcc
	v_cmp_class_f32_e32 vcc, v0, v208
	s_nop 1
	v_cndmask_b32_e32 v69, v1, v0, vcc
	v_div_scale_f32 v16, s[2:3], v69, v69, 1.0
	v_rcp_f32_e32 v206, v16
	s_waitcnt vmcnt(27)
	v_mfma_f32_32x32x16_f16 v[0:15], v[84:87], v[96:99], 0
	ds_read_b128 v[84:87], v127 offset:10240
	s_mov_b32 s2, 0xa000
	v_fma_f32 v17, -v16, v206, 1.0
	v_fmac_f32_e32 v206, v17, v206
	v_div_scale_f32 v17, vcc, 1.0, v69, 1.0
	v_mul_f32_e32 v70, v17, v206
	v_fma_f32 v18, -v16, v70, v17
	v_fmac_f32_e32 v70, v18, v206
	v_fma_f32 v71, -v16, v70, v17
	s_waitcnt vmcnt(26)
	v_mfma_f32_32x32x16_f16 v[16:31], v[92:95], v[96:99], 0
	ds_read_b128 v[92:95], v127 offset:10272
	v_div_fmas_f32 v70, v71, v206, v70
	v_div_fixup_f32 v70, v70, v69, 1.0
	v_mul_f32_e64 v210, v118, v70
	v_mul_f32_e64 v211, v119, v70
	v_pk_mul_f32 v[206:207], v[74:75], v[70:71] op_sel_hi:[1,0]
	v_pk_mul_f32 v[74:75], v[202:203], v[70:71] op_sel_hi:[1,0]
	s_waitcnt vmcnt(15)
	v_pk_fma_f32 v[36:37], v[210:211], v[36:37], v[88:89]
	s_waitcnt lgkmcnt(1)
	v_mfma_f32_32x32x16_f16 v[0:15], v[76:79], v[84:87], v[0:15]
	v_fma_f32 v34, v74, v34, v50
	v_fma_f32 v35, v75, v35, v51
	v_fma_f32 v38, v206, v38, v90
	v_fma_f32 v39, v207, v39, v91
	v_cvt_pk_f16_f32 v50, v36, v37
	v_pk_mul_f32 v[36:37], v[154:155], v[70:71] op_sel_hi:[1,0]
	v_cvt_pk_f16_f32 v51, v38, v39
	v_pk_mul_f32 v[38:39], v[186:187], v[70:71] op_sel_hi:[1,0]
	s_waitcnt vmcnt(13)
	v_pk_fma_f32 v[36:37], v[36:37], v[130:131], v[138:139]
	v_mfma_f32_32x32x16_f16 v[16:31], v[120:123], v[84:87], v[16:31]
	ds_read_b128 v[84:87], v127 offset:10336
	v_mul_f32_e64 v72, v72, v70
	v_mul_f32_e64 v73, v73, v70
	v_mul_f32_e64 v88, v184, v70
	v_mul_f32_e64 v89, v185, v70
	v_pk_fma_f32 v[32:33], v[72:73], v[32:33], v[48:49]
	v_cvt_pk_f16_f32 v49, v34, v35
	v_cvt_pk_f16_f32 v48, v32, v33
	v_pk_mul_f32 v[32:33], v[190:191], v[70:71] op_sel_hi:[1,0]
	s_waitcnt lgkmcnt(1)
	v_mfma_f32_32x32x16_f16 v[0:15], v[60:63], v[92:95], v[0:15]
	v_fma_f32 v60, v38, v128, v136
	v_fma_f32 v61, v39, v129, v137
	v_mul_f32_e64 v62, v204, v70
	v_mul_f32_e64 v63, v205, v70
	v_mul_f32_e64 v34, v194, v70
	v_mul_f32_e64 v35, v195, v70
	s_waitcnt vmcnt(8)
	v_pk_fma_f32 v[62:63], v[62:63], v[140:141], v[148:149]
	v_pk_fma_f32 v[40:41], v[34:35], v[40:41], v[132:133]
	v_pk_fma_f32 v[42:43], v[32:33], v[42:43], v[134:135]
	global_load_dwordx4 v[116:119], v82, s[30:31]
	global_load_dwordx4 v[72:75], v82, s[30:31] offset:32
	v_mfma_f32_32x32x16_f16 v[16:31], v[52:55], v[92:95], v[16:31]
	v_cvt_pk_f16_f32 v55, v36, v37
	ds_read_b128 v[36:39], v127 offset:10304
	v_cvt_pk_f16_f32 v54, v60, v61
	v_mul_f32_e64 v60, v200, v70
	v_mul_f32_e64 v61, v201, v70
	global_load_dwordx4 v[76:79], v82, s[30:31] offset:64
	global_load_dwordx4 v[32:35], v82, s[30:31] offset:96
	v_pk_fma_f32 v[60:61], v[60:61], v[142:143], v[150:151]
	s_waitcnt lgkmcnt(0)
	v_mfma_f32_32x32x16_f16 v[0:15], v[56:59], v[36:39], v[0:15]
	v_mul_f32_e64 v56, v196, v70
	v_mul_f32_e64 v57, v197, v70
	v_mul_f32_e64 v58, v198, v70
	v_mul_f32_e64 v59, v199, v70
	v_cvt_pk_f16_f32 v53, v42, v43
	v_cvt_pk_f16_f32 v52, v40, v41
	global_load_dwordx4 v[40:43], v82, s[30:31] offset:128
	v_mfma_f32_32x32x16_f16 v[16:31], v[44:47], v[36:39], v[16:31]
	s_waitcnt vmcnt(11)
	v_fma_f32 v38, v56, v146, v166
	v_fma_f32 v39, v57, v147, v167
	v_cvt_pk_f16_f32 v57, v60, v61
	v_mul_f32_e64 v60, v188, v70
	v_mul_f32_e64 v61, v189, v70
	v_cvt_pk_f16_f32 v56, v62, v63
	v_pk_mul_f32 v[62:63], v[124:125], v[70:71] op_sel_hi:[1,0]
	s_waitcnt vmcnt(10)
	v_pk_fma_f32 v[60:61], v[60:61], v[162:163], v[170:171]
	v_add_co_u32_e32 v170, vcc, s2, v156
	v_mfma_f32_32x32x16_f16 v[0:15], v[64:67], v[84:87], v[0:15]
	v_mul_f32_e64 v64, v192, v70
	v_mul_f32_e64 v65, v193, v70
	v_fma_f32 v36, v58, v144, v164
	v_fma_f32 v37, v59, v145, v165
	v_fma_f32 v136, v64, v160, v168
	v_fma_f32 v137, v65, v161, v169
	s_waitcnt vmcnt(5)
	v_pk_fma_f32 v[70:71], v[88:89], v[176:177], v[180:181]
	v_pk_fma_f32 v[62:63], v[62:63], v[178:179], v[182:183]
	v_addc_co_u32_e32 v171, vcc, 0, v157, vcc
	v_mfma_f32_32x32x16_f16 v[16:31], v[172:175], v[84:87], v[16:31]
	global_load_dwordx4 v[44:47], v82, s[30:31] offset:160
	v_cvt_pk_f16_f32 v59, v38, v39
	v_cvt_pk_f16_f32 v58, v36, v37
	global_load_dwordx4 v[36:39], v82, s[30:31] offset:192
	v_cvt_pk_f16_f32 v63, v62, v63
	v_cvt_pk_f16_f32 v62, v70, v71
	s_movk_i32 s2, 0x7000
	s_nop 4
	v_add_f32_e32 v64, v0, v16
	v_add_f32_e32 v64, 0, v64
	v_add_f32_e32 v65, v1, v17
	v_add_f32_e32 v64, v65, v64
	v_add_f32_e32 v65, v2, v18
	v_add_f32_e32 v64, v65, v64
	v_add_f32_e32 v65, v3, v19
	v_add_f32_e32 v64, v65, v64
	v_add_f32_e32 v65, v4, v20
	v_add_f32_e32 v64, v65, v64
	v_add_f32_e32 v65, v5, v21
	v_add_f32_e32 v66, v65, v64
	v_pk_add_f32 v[64:65], v[6:7], v[22:23]
	v_add_co_u32_e32 v184, vcc, s2, v156
	v_add_f32_e32 v64, v64, v66
	v_add_f32_e32 v66, v65, v64
	v_pk_add_f32 v[64:65], v[8:9], v[24:25]
	v_addc_co_u32_e32 v185, vcc, 0, v157, vcc
	v_add_f32_e32 v64, v64, v66
	v_add_f32_e32 v66, v65, v64
	v_pk_add_f32 v[64:65], v[10:11], v[26:27]
	s_movk_i32 s2, 0x6000
	v_add_f32_e32 v64, v64, v66
	v_add_f32_e32 v66, v65, v64
	v_pk_add_f32 v[64:65], v[12:13], v[28:29]
	v_add_co_u32_e32 v186, vcc, s2, v156
	v_add_f32_e32 v64, v64, v66
	v_add_f32_e32 v66, v65, v64
	v_pk_add_f32 v[64:65], v[14:15], v[30:31]
	v_addc_co_u32_e32 v187, vcc, 0, v157, vcc
	v_add_f32_e32 v64, v64, v66
	v_add_f32_e32 v69, v65, v64
	ds_bpermute_b32 v84, v209, v69
	global_load_dwordx4 v[64:67], v82, s[30:31] offset:224
	v_cvt_pk_f16_f32 v61, v60, v61
	v_cvt_pk_f16_f32 v60, v136, v137
	s_waitcnt lgkmcnt(0)
	v_add_f32_e32 v69, v69, v84
	v_mul_f32_e32 v92, 0x3c800000, v69
	v_ashrrev_i32_e32 v69, 31, v68
	v_lshl_add_u64 v[68:69], v[68:69], 2, s[24:25]
	v_lshl_add_u64 v[124:125], v[68:69], 0, v[82:83]
	global_load_dwordx4 v[140:143], v[124:125], off
	global_load_dwordx4 v[88:91], v[124:125], off offset:32
	global_load_dwordx4 v[84:87], v[124:125], off offset:64
	global_load_dwordx4 v[68:71], v[124:125], off offset:96
	v_pk_add_f32 v[180:181], v[10:11], v[92:93] op_sel_hi:[1,0] neg_lo:[0,1] neg_hi:[0,1]
	v_pk_add_f32 v[182:183], v[8:9], v[92:93] op_sel_hi:[1,0] neg_lo:[0,1] neg_hi:[0,1]
	v_pk_add_f32 v[8:9], v[2:3], v[92:93] op_sel_hi:[1,0] neg_lo:[0,1] neg_hi:[0,1]
	v_pk_add_f32 v[10:11], v[0:1], v[92:93] op_sel_hi:[1,0] neg_lo:[0,1] neg_hi:[0,1]
	global_load_dwordx4 v[0:3], v[170:171], off offset:-4096
	v_pk_add_f32 v[178:179], v[12:13], v[92:93] op_sel_hi:[1,0] neg_lo:[0,1] neg_hi:[0,1]
	v_pk_add_f32 v[174:175], v[16:17], v[92:93] op_sel_hi:[1,0] neg_lo:[0,1] neg_hi:[0,1]
	v_fma_f32 v12, v10, v10, 0
	v_fmac_f32_e32 v12, v174, v174
	v_fmac_f32_e32 v12, v11, v11
	v_fmac_f32_e32 v12, v175, v175
	v_pk_add_f32 v[172:173], v[18:19], v[92:93] op_sel_hi:[1,0] neg_lo:[0,1] neg_hi:[0,1]
	v_fmac_f32_e32 v12, v8, v8
	global_load_dwordx4 v[144:147], v[152:153], off
	global_load_dwordx4 v[148:151], v[152:153], off offset:2048
	v_fmac_f32_e32 v12, v172, v172
	v_fmac_f32_e32 v12, v9, v9
	v_pk_add_f32 v[4:5], v[4:5], v[92:93] op_sel_hi:[1,0] neg_lo:[0,1] neg_hi:[0,1]
	v_fmac_f32_e32 v12, v173, v173
	v_pk_add_f32 v[168:169], v[20:21], v[92:93] op_sel_hi:[1,0] neg_lo:[0,1] neg_hi:[0,1]
	v_fmac_f32_e32 v12, v4, v4
	v_fmac_f32_e32 v12, v168, v168
	v_fmac_f32_e32 v12, v5, v5
	v_pk_add_f32 v[6:7], v[6:7], v[92:93] op_sel_hi:[1,0] neg_lo:[0,1] neg_hi:[0,1]
	v_fmac_f32_e32 v12, v169, v169
	v_pk_add_f32 v[166:167], v[22:23], v[92:93] op_sel_hi:[1,0] neg_lo:[0,1] neg_hi:[0,1]
	v_fmac_f32_e32 v12, v6, v6
	v_fmac_f32_e32 v12, v166, v166
	v_fmac_f32_e32 v12, v7, v7
	v_fmac_f32_e32 v12, v167, v167
	v_pk_add_f32 v[164:165], v[24:25], v[92:93] op_sel_hi:[1,0] neg_lo:[0,1] neg_hi:[0,1]
	v_fmac_f32_e32 v12, v182, v182
	v_fmac_f32_e32 v12, v164, v164
	v_fmac_f32_e32 v12, v183, v183
	v_fmac_f32_e32 v12, v165, v165
	v_pk_add_f32 v[162:163], v[26:27], v[92:93] op_sel_hi:[1,0] neg_lo:[0,1] neg_hi:[0,1]
	v_fmac_f32_e32 v12, v180, v180
	v_fmac_f32_e32 v12, v162, v162
	v_fmac_f32_e32 v12, v181, v181
	v_fmac_f32_e32 v12, v163, v163
	v_pk_add_f32 v[160:161], v[28:29], v[92:93] op_sel_hi:[1,0] neg_lo:[0,1] neg_hi:[0,1]
	v_fmac_f32_e32 v12, v178, v178
	v_fmac_f32_e32 v12, v160, v160
	v_pk_add_f32 v[154:155], v[30:31], v[92:93] op_sel_hi:[1,0] neg_lo:[0,1] neg_hi:[0,1]
	v_pk_add_f32 v[176:177], v[14:15], v[92:93] op_sel_hi:[1,0] neg_lo:[0,1] neg_hi:[0,1]
	v_fmac_f32_e32 v12, v179, v179
	global_load_dwordx4 v[92:95], v[184:185], off offset:-4096
	global_load_dwordx4 v[28:31], v[124:125], off offset:128
	global_load_dwordx4 v[20:23], v[124:125], off offset:160
	v_fmac_f32_e32 v12, v161, v161
	v_fmac_f32_e32 v12, v176, v176
	global_load_dwordx4 v[120:123], v[186:187], off offset:2048
	v_fmac_f32_e32 v12, v154, v154
	v_fmac_f32_e32 v12, v177, v177
	v_fmac_f32_e32 v12, v155, v155
	ds_bpermute_b32 v13, v209, v12
	s_waitcnt lgkmcnt(0)
	v_add_f32_e32 v12, v12, v13
	v_fmac_f32_e32 v126, 0x3c800000, v12
	v_mul_f32_e32 v12, 0x4f800000, v126
	v_cmp_gt_f32_e32 vcc, s8, v126
	s_nop 1
	v_cndmask_b32_e32 v12, v126, v12, vcc
	global_load_dwordx4 v[24:27], v[124:125], off offset:192
	global_load_dwordx4 v[16:19], v[124:125], off offset:224
	s_nop 0
	global_load_dwordx4 v[124:127], v[184:185], off
	global_load_dwordx4 v[128:131], v[184:185], off offset:2048
	v_sqrt_f32_e32 v13, v12
	s_nop 0
	v_add_u32_e32 v14, -1, v13
	v_fma_f32 v15, -v14, v13, v12
	v_cmp_ge_f32_e64 s[2:3], 0, v15
	v_add_u32_e32 v15, 1, v13
	s_nop 0
	v_cndmask_b32_e64 v14, v13, v14, s[2:3]
	v_fma_f32 v13, -v15, v13, v12
	v_cmp_lt_f32_e64 s[2:3], 0, v13
	s_nop 1
	v_cndmask_b32_e64 v13, v14, v15, s[2:3]
	v_mul_f32_e32 v14, 0x37800000, v13
	s_mov_b32 s2, 0x8000
	v_cndmask_b32_e32 v13, v13, v14, vcc
	v_add_co_u32_e32 v188, vcc, s2, v156
	s_nop 1
	v_addc_co_u32_e32 v189, vcc, 0, v157, vcc
	v_cmp_class_f32_e32 vcc, v12, v208
	global_load_dwordx4 v[132:135], v[188:189], off
	global_load_dwordx4 v[136:139], v[188:189], off offset:2048
	v_cndmask_b32_e32 v12, v13, v12, vcc
	v_div_scale_f32 v13, s[2:3], v12, v12, 1.0
	v_rcp_f32_e32 v14, v13
	s_mov_b32 s2, 0x9000
	s_mov_b32 s3, 0xbc90
	v_fma_f32 v15, -v13, v14, 1.0
	v_fmac_f32_e32 v14, v15, v14
	v_div_scale_f32 v15, vcc, 1.0, v12, 1.0
	v_mul_f32_e32 v82, v15, v14
	v_fma_f32 v190, -v13, v82, v15
	v_fmac_f32_e32 v82, v190, v14
	v_fma_f32 v13, -v13, v82, v15
	v_div_fmas_f32 v13, v13, v14, v82
	v_div_fixup_f32 v82, v13, v12, 1.0
	v_pk_mul_f32 v[190:191], v[6:7], v[82:83] op_sel_hi:[1,0]
	v_pk_mul_f32 v[192:193], v[4:5], v[82:83] op_sel_hi:[1,0]
	v_pk_mul_f32 v[4:5], v[8:9], v[82:83] op_sel_hi:[1,0]
	v_pk_mul_f32 v[6:7], v[10:11], v[82:83] op_sel_hi:[1,0]
	s_waitcnt vmcnt(16)
	v_pk_fma_f32 v[118:119], v[4:5], v[118:119], v[142:143]
	v_pk_fma_f32 v[116:117], v[6:7], v[116:117], v[140:141]
	s_waitcnt vmcnt(12)
	v_mfma_f32_32x32x16_f16 v[0:15], v[0:3], v[96:99], 0
	v_fma_f32 v72, v192, v72, v88
	v_fma_f32 v73, v193, v73, v89
	v_fma_f32 v74, v190, v74, v90
	v_fma_f32 v75, v191, v75, v91
	global_load_dwordx4 v[88:91], v[152:153], off offset:1024
	v_cvt_pk_f16_f32 v75, v74, v75
	v_cvt_pk_f16_f32 v74, v72, v73
	v_cvt_pk_f16_f32 v73, v118, v119
	v_pk_mul_f32 v[118:119], v[178:179], v[82:83] op_sel_hi:[1,0]
	s_waitcnt vmcnt(12)
	v_mfma_f32_32x32x16_f16 v[0:15], v[144:147], v[104:107], v[0:15]
	v_mul_f32_e64 v144, v180, v82
	v_mul_f32_e64 v145, v181, v82
	v_mul_f32_e64 v146, v182, v82
	v_mul_f32_e64 v147, v183, v82
	v_fma_f32 v144, v144, v78, v86
	v_fma_f32 v145, v145, v79, v87
	v_pk_fma_f32 v[146:147], v[146:147], v[76:77], v[84:85]
	global_load_dwordx4 v[84:87], v[152:153], off offset:3072
	v_add_co_u32_e32 v152, vcc, s2, v156
	s_waitcnt vmcnt(12)
	v_mfma_f32_32x32x16_f16 v[0:15], v[148:151], v[100:103], v[0:15]
	v_addc_co_u32_e32 v153, vcc, 0, v157, vcc
	v_fma_f32 v32, v118, v32, v68
	v_fma_f32 v33, v119, v33, v69
	v_cvt_pk_f16_f32 v69, v144, v145
	v_cvt_pk_f16_f32 v68, v146, v147
	global_load_dwordx4 v[144:147], v[186:187], off offset:3072
	global_load_dwordx4 v[148:151], v[184:185], off offset:3072
	s_waitcnt vmcnt(13)
	v_mfma_f32_32x32x16_f16 v[0:15], v[92:95], v[112:115], v[0:15]
	global_load_dwordx4 v[92:95], v[152:153], off offset:1024
	global_load_dwordx4 v[76:79], v[170:171], off offset:3072
	v_cvt_pk_f16_f32 v72, v116, v117
	v_mul_f32_e64 v116, v176, v82
	v_mul_f32_e64 v117, v177, v82
	v_pk_mul_f32 v[118:119], v[174:175], v[82:83] op_sel_hi:[1,0]
	v_pk_fma_f32 v[34:35], v[116:117], v[34:35], v[70:71]
	v_pk_mul_f32 v[116:117], v[172:173], v[82:83] op_sel_hi:[1,0]
	s_waitcnt vmcnt(12)
	v_mfma_f32_32x32x16_f16 v[0:15], v[120:123], v[108:111], v[0:15]
	global_load_dwordx4 v[120:123], v[184:185], off offset:1024
	v_fma_f32 v28, v118, v40, v28
	v_fma_f32 v29, v119, v41, v29
	v_fma_f32 v30, v116, v42, v30
	v_fma_f32 v31, v117, v43, v31
	v_cvt_pk_f16_f32 v40, v28, v29
	v_cvt_pk_f16_f32 v41, v30, v31
	v_pk_mul_f32 v[28:29], v[162:163], v[82:83] op_sel_hi:[1,0]
	v_pk_mul_f32 v[30:31], v[164:165], v[82:83] op_sel_hi:[1,0]
	s_waitcnt vmcnt(10)
	v_mfma_f32_32x32x16_f16 v[0:15], v[124:127], v[48:51], v[0:15]
	v_fma_f32 v24, v30, v36, v24
	v_fma_f32 v25, v31, v37, v25
	v_fma_f32 v26, v28, v38, v26
	v_fma_f32 v27, v29, v39, v27
	global_load_dwordx4 v[36:39], v[188:189], off offset:1024
	v_cvt_pk_f16_f32 v71, v34, v35
	v_cvt_pk_f16_f32 v70, v32, v33
	v_pk_mul_f32 v[32:33], v[166:167], v[82:83] op_sel_hi:[1,0]
	v_pk_mul_f32 v[34:35], v[168:169], v[82:83] op_sel_hi:[1,0]
	s_waitcnt vmcnt(10)
	v_mfma_f32_32x32x16_f16 v[0:15], v[128:131], v[52:55], v[0:15]
	global_load_dwordx4 v[126:129], v[186:187], off offset:1024
	v_fma_f32 v20, v34, v44, v20
	v_fma_f32 v21, v35, v45, v21
	v_fma_f32 v22, v32, v46, v22
	v_fma_f32 v23, v33, v47, v23
	v_cvt_pk_f16_f32 v42, v20, v21
	v_cvt_pk_f16_f32 v43, v22, v23
	v_pk_mul_f32 v[20:21], v[154:155], v[82:83] op_sel_hi:[1,0]
	v_pk_mul_f32 v[22:23], v[160:161], v[82:83] op_sel_hi:[1,0]
	s_waitcnt vmcnt(10)
	v_mfma_f32_32x32x16_f16 v[0:15], v[132:135], v[56:59], v[0:15]
	v_fma_f32 v16, v22, v64, v16
	v_fma_f32 v17, v23, v65, v17
	v_fma_f32 v18, v20, v66, v18
	v_fma_f32 v19, v21, v67, v19
	global_load_dwordx4 v[64:67], v[188:189], off offset:3072
	s_mov_b32 s2, 0xa714
	v_mov_b32_e32 v164, 0xb7d0
	v_cvt_pk_f16_f32 v34, v16, v17
	v_cvt_pk_f16_f32 v35, v18, v19
	s_waitcnt vmcnt(10)
	v_mfma_f32_32x32x16_f16 v[0:15], v[136:139], v[60:63], v[0:15]
	v_cvt_pk_f16_f32 v33, v26, v27
	v_cvt_pk_f16_f32 v32, v24, v25
	global_load_dwordx4 v[132:135], v[152:153], off offset:2048
	v_add_co_u32_e32 v136, vcc, s6, v156
	global_load_dwordx4 v[140:143], v[170:171], off
	global_load_dwordx4 v[44:47], v[152:153], off offset:3072
	s_nop 5
	v_cvt_pk_f16_f32 v0, v0, v1
	v_and_b32_e32 v1, 0x7fff7fff, v0
	v_cvt_pk_f16_f32 v2, v2, v3
	v_pk_fma_f16 v16, v1, s2, v164 op_sel_hi:[1,0,0]
	v_and_b32_e32 v3, 0x7fff7fff, v2
	v_pk_fma_f16 v16, v16, v1, s3 op_sel_hi:[1,1,0]
	v_pk_fma_f16 v18, v3, s2, v164 op_sel_hi:[1,0,0]
	v_pk_mul_f16 v16, v1, v16
	v_pk_fma_f16 v18, v18, v3, s3 op_sel_hi:[1,1,0]
	v_exp_f16_e32 v17, v16
	v_exp_f16_sdwa v16, v16 dst_sel:DWORD dst_unused:UNUSED_PAD src0_sel:WORD_1
	v_pk_mul_f16 v18, v3, v18
	v_pk_add_f16 v0, v1, v0
	v_exp_f16_e32 v19, v18
	v_exp_f16_sdwa v18, v18 dst_sel:DWORD dst_unused:UNUSED_PAD src0_sel:WORD_1
	v_pack_b32_f16 v16, v17, v16
	v_pk_fma_f16 v116, v1, v16, v0 neg_lo:[1,0,0] neg_hi:[1,0,0]
	v_pk_add_f16 v1, v3, v2
	v_pack_b32_f16 v0, v19, v18
	v_pk_fma_f16 v117, v3, v0, v1 neg_lo:[1,0,0] neg_hi:[1,0,0]
	v_cvt_pk_f16_f32 v0, v4, v5
	v_and_b32_e32 v1, 0x7fff7fff, v0
	v_pk_fma_f16 v2, v1, s2, v164 op_sel_hi:[1,0,0]
	s_waitcnt vmcnt(8)
	v_mfma_f32_32x32x16_f16 v[16:31], v[92:95], v[96:99], 0
	v_pk_fma_f16 v2, v2, v1, s3 op_sel_hi:[1,1,0]
	v_cvt_pk_f16_f32 v4, v6, v7
	v_pk_mul_f16 v2, v1, v2
	v_and_b32_e32 v5, 0x7fff7fff, v4
	v_exp_f16_e32 v3, v2
	v_exp_f16_sdwa v2, v2 dst_sel:DWORD dst_unused:UNUSED_PAD src0_sel:WORD_1
	v_pk_fma_f16 v6, v5, s2, v164 op_sel_hi:[1,0,0]
	v_pk_add_f16 v0, v1, v0
	v_pk_fma_f16 v6, v6, v5, s3 op_sel_hi:[1,1,0]
	v_pack_b32_f16 v2, v3, v2
	v_pk_mul_f16 v6, v5, v6
	v_pk_fma_f16 v118, v1, v2, v0 neg_lo:[1,0,0] neg_hi:[1,0,0]
	v_cvt_pk_f16_f32 v1, v8, v9
	v_exp_f16_e32 v7, v6
	v_exp_f16_sdwa v6, v6 dst_sel:DWORD dst_unused:UNUSED_PAD src0_sel:WORD_1
	v_and_b32_e32 v2, 0x7fff7fff, v1
	v_pk_fma_f16 v3, v2, s2, v164 op_sel_hi:[1,0,0]
	v_mfma_f32_32x32x16_f16 v[16:31], v[88:91], v[104:107], v[16:31]
	v_pk_fma_f16 v3, v3, v2, s3 op_sel_hi:[1,1,0]
	v_pack_b32_f16 v0, v7, v6
	v_pk_mul_f16 v3, v2, v3
	v_pk_add_f16 v4, v5, v4
	v_exp_f16_e32 v6, v3
	v_exp_f16_sdwa v3, v3 dst_sel:DWORD dst_unused:UNUSED_PAD src0_sel:WORD_1
	v_pk_fma_f16 v119, v5, v0, v4 neg_lo:[1,0,0] neg_hi:[1,0,0]
	v_cvt_pk_f16_f32 v4, v10, v11
	v_pk_add_f16 v1, v2, v1
	v_pack_b32_f16 v0, v6, v3
	v_and_b32_e32 v5, 0x7fff7fff, v4
	v_pk_fma_f16 v124, v2, v0, v1 neg_lo:[1,0,0] neg_hi:[1,0,0]
	v_pk_fma_f16 v0, v5, s2, v164 op_sel_hi:[1,0,0]
	v_mfma_f32_32x32x16_f16 v[16:31], v[84:87], v[100:103], v[16:31]
	v_pk_fma_f16 v0, v0, v5, s3 op_sel_hi:[1,1,0]
	v_addc_co_u32_e32 v137, vcc, 0, v157, vcc
	v_pk_mul_f16 v0, v5, v0
	global_load_dwordx4 v[84:87], v[170:171], off offset:2048
	v_exp_f16_e32 v6, v0
	v_exp_f16_sdwa v7, v0 dst_sel:DWORD dst_unused:UNUSED_PAD src0_sel:WORD_1
	global_load_dwordx4 v[0:3], v[136:137], off offset:2048
	s_waitcnt vmcnt(6)
	v_mfma_f32_32x32x16_f16 v[16:31], v[126:129], v[112:115], v[16:31]
	s_mov_b32 s6, 0xb000
	v_cvt_pk_f16_f32 v8, v12, v13
	v_and_b32_e32 v9, 0x7fff7fff, v8
	v_pk_fma_f16 v10, v9, s2, v164 op_sel_hi:[1,0,0]
	v_pack_b32_f16 v6, v6, v7
	v_pk_fma_f16 v10, v10, v9, s3 op_sel_hi:[1,1,0]
	v_pk_add_f16 v4, v5, v4
	v_mfma_f32_32x32x16_f16 v[16:31], v[144:147], v[108:111], v[16:31]
	v_pk_mul_f16 v10, v9, v10
	v_pk_fma_f16 v125, v5, v6, v4 neg_lo:[1,0,0] neg_hi:[1,0,0]
	v_exp_f16_e32 v11, v10
	v_exp_f16_sdwa v10, v10 dst_sel:DWORD dst_unused:UNUSED_PAD src0_sel:WORD_1
	v_pk_add_f16 v5, v9, v8
	v_pack_b32_f16 v4, v11, v10
	v_mfma_f32_32x32x16_f16 v[16:31], v[120:123], v[48:51], v[16:31]
	v_pk_fma_f16 v126, v9, v4, v5 neg_lo:[1,0,0] neg_hi:[1,0,0]
	v_cvt_pk_f16_f32 v4, v14, v15
	v_and_b32_e32 v5, 0x7fff7fff, v4
	v_pk_fma_f16 v6, v5, s2, v164 op_sel_hi:[1,0,0]
	v_pk_add_f16 v4, v5, v4
	v_pk_fma_f16 v6, v6, v5, s3 op_sel_hi:[1,1,0]
	v_mfma_f32_32x32x16_f16 v[16:31], v[148:151], v[52:55], v[16:31]
	v_add_co_u32_e32 v150, vcc, s7, v156
	v_pk_mul_f16 v6, v5, v6
	s_nop 0
	v_addc_co_u32_e32 v151, vcc, 0, v157, vcc
	global_load_dwordx4 v[88:91], v[150:151], off offset:-4096
	v_add_co_u32_e32 v152, vcc, s6, v156
	v_mfma_f32_32x32x16_f16 v[16:31], v[36:39], v[56:59], v[16:31]
	s_nop 0
	v_addc_co_u32_e32 v153, vcc, 0, v157, vcc
	global_load_dwordx4 v[92:95], v[152:153], off offset:2048
	global_load_dwordx4 v[146:149], v[152:153], off offset:3072
	global_load_dwordx4 v[120:123], v[150:151], off offset:2048
	global_load_dwordx4 v[166:169], v[150:151], off offset:1024
	v_exp_f16_e32 v7, v6
	s_waitcnt vmcnt(10)
	v_mfma_f32_32x32x16_f16 v[16:31], v[64:67], v[60:63], v[16:31]
	global_load_dwordx4 v[64:67], v[150:151], off
	v_exp_f16_sdwa v6, v6 dst_sel:DWORD dst_unused:UNUSED_PAD src0_sel:WORD_1
	s_mov_b32 s6, 0xe000
	v_add_co_u32_e32 v138, vcc, s6, v156
	v_pack_b32_f16 v6, v7, v6
	v_pk_fma_f16 v127, v5, v6, v4 neg_lo:[1,0,0] neg_hi:[1,0,0]
	s_nop 5
	v_cvt_pk_f16_f32 v8, v16, v17
	v_and_b32_e32 v9, 0x7fff7fff, v8
	v_pk_fma_f16 v10, v9, s2, v164 op_sel_hi:[1,0,0]
	v_pk_add_f16 v5, v9, v8
	v_pk_fma_f16 v10, v10, v9, s3 op_sel_hi:[1,1,0]
	v_addc_co_u32_e32 v139, vcc, 0, v157, vcc
	v_pk_mul_f16 v10, v9, v10
	v_cvt_pk_f16_f32 v8, v20, v21
	v_exp_f16_e32 v11, v10
	v_exp_f16_sdwa v10, v10 dst_sel:DWORD dst_unused:UNUSED_PAD src0_sel:WORD_1
	v_and_b32_e32 v20, 0x7fff7fff, v8
	v_pk_add_f16 v82, v20, v8
	global_load_dwordx4 v[36:39], v[136:137], off offset:1024
	v_pack_b32_f16 v4, v11, v10
	v_pk_fma_f16 v128, v9, v4, v5 neg_lo:[1,0,0] neg_hi:[1,0,0]
	v_cvt_pk_f16_f32 v4, v18, v19
	global_load_dwordx4 v[16:19], v[138:139], off offset:-4096
	v_and_b32_e32 v5, 0x7fff7fff, v4
	v_pk_fma_f16 v6, v5, s2, v164 op_sel_hi:[1,0,0]
	v_pk_fma_f16 v9, v20, s2, v164 op_sel_hi:[1,0,0]
	v_pk_fma_f16 v6, v6, v5, s3 op_sel_hi:[1,1,0]
	v_pk_fma_f16 v9, v9, v20, s3 op_sel_hi:[1,1,0]
	v_pk_mul_f16 v6, v5, v6
	v_pk_mul_f16 v9, v20, v9
	v_exp_f16_e32 v7, v6
	v_exp_f16_sdwa v6, v6 dst_sel:DWORD dst_unused:UNUSED_PAD src0_sel:WORD_1
	v_exp_f16_e32 v10, v9
	v_exp_f16_sdwa v9, v9 dst_sel:DWORD dst_unused:UNUSED_PAD src0_sel:WORD_1
	v_pk_add_f16 v4, v5, v4
	v_pack_b32_f16 v6, v7, v6
	v_pk_fma_f16 v129, v5, v6, v4 neg_lo:[1,0,0] neg_hi:[1,0,0]
	v_pack_b32_f16 v21, v10, v9
	s_waitcnt vmcnt(8)
	v_mfma_f32_32x32x16_f16 v[0:15], v[0:3], v[96:99], 0
	v_pk_fma_f16 v130, v20, v21, v82 neg_lo:[1,0,0] neg_hi:[1,0,0]
	v_cvt_pk_f16_f32 v82, v22, v23
	v_and_b32_e32 v131, 0x7fff7fff, v82
	v_pk_fma_f16 v20, v131, s2, v164 op_sel_hi:[1,0,0]
	v_cvt_pk_f16_f32 v24, v24, v25
	v_pk_fma_f16 v20, v20, v131, s3 op_sel_hi:[1,1,0]
	v_and_b32_e32 v25, 0x7fff7fff, v24
	v_pk_mul_f16 v20, v131, v20
	v_mfma_f32_32x32x16_f16 v[0:15], v[132:135], v[104:107], v[0:15]
	v_exp_f16_e32 v144, v20
	v_exp_f16_sdwa v132, v20 dst_sel:DWORD dst_unused:UNUSED_PAD src0_sel:WORD_1
	v_pk_fma_f16 v20, v25, s2, v164 op_sel_hi:[1,0,0]
	global_load_dwordx4 v[152:155], v[152:153], off offset:1024
	v_pk_fma_f16 v20, v20, v25, s3 op_sel_hi:[1,1,0]
	v_pack_b32_f16 v132, v144, v132
	v_pk_mul_f16 v133, v25, v20
	global_load_dwordx4 v[20:23], v[136:137], off offset:3072
	v_mfma_f32_32x32x16_f16 v[0:15], v[140:143], v[100:103], v[0:15]
	global_load_dwordx4 v[142:145], v[170:171], off offset:1024
	v_cvt_pk_f16_f32 v26, v26, v27
	v_and_b32_e32 v27, 0x7fff7fff, v26
	v_exp_f16_e32 v134, v133
	v_exp_f16_sdwa v133, v133 dst_sel:DWORD dst_unused:UNUSED_PAD src0_sel:WORD_1
	v_pk_add_f16 v82, v131, v82
	v_pk_add_f16 v24, v25, v24
	v_mfma_f32_32x32x16_f16 v[0:15], v[84:87], v[112:115], v[0:15]
	v_pk_fma_f16 v84, v27, s2, v164 op_sel_hi:[1,0,0]
	v_pk_fma_f16 v131, v131, v132, v82 neg_lo:[1,0,0] neg_hi:[1,0,0]
	v_pk_fma_f16 v84, v84, v27, s3 op_sel_hi:[1,1,0]
	v_pack_b32_f16 v82, v134, v133
	v_pk_mul_f16 v84, v27, v84
	v_pk_fma_f16 v132, v25, v82, v24 neg_lo:[1,0,0] neg_hi:[1,0,0]
	v_exp_f16_e32 v85, v84
	s_waitcnt vmcnt(10)
	v_mfma_f32_32x32x16_f16 v[0:15], v[88:91], v[108:111], v[0:15]
	v_exp_f16_sdwa v84, v84 dst_sel:DWORD dst_unused:UNUSED_PAD src0_sel:WORD_1
	v_pk_add_f16 v25, v27, v26
	global_load_dwordx4 v[170:173], v[150:151], off offset:3072
	s_mov_b32 s6, 0x13000
	v_pack_b32_f16 v24, v85, v84
	v_pk_fma_f16 v133, v27, v24, v25 neg_lo:[1,0,0] neg_hi:[1,0,0]
	v_cvt_pk_f16_f32 v24, v28, v29
	s_waitcnt vmcnt(10)
	v_mfma_f32_32x32x16_f16 v[0:15], v[92:95], v[72:75], v[0:15]
	v_and_b32_e32 v25, 0x7fff7fff, v24
	v_cvt_pk_f16_f32 v28, v30, v31
	v_pk_fma_f16 v26, v25, s2, v164 op_sel_hi:[1,0,0]
	v_and_b32_e32 v29, 0x7fff7fff, v28
	v_pk_fma_f16 v26, v26, v25, s3 op_sel_hi:[1,1,0]
	v_pk_fma_f16 v30, v29, s2, v164 op_sel_hi:[1,0,0]
	v_pk_mul_f16 v26, v25, v26
	s_waitcnt vmcnt(6)
	v_mfma_f32_32x32x16_f16 v[0:15], v[64:67], v[68:71], v[0:15]
	v_pk_fma_f16 v30, v30, v29, s3 op_sel_hi:[1,1,0]
	v_exp_f16_e32 v27, v26
	v_exp_f16_sdwa v26, v26 dst_sel:DWORD dst_unused:UNUSED_PAD src0_sel:WORD_1
	v_pk_mul_f16 v30, v29, v30
	v_pk_add_f16 v24, v25, v24
	v_exp_f16_e32 v31, v30
	v_exp_f16_sdwa v30, v30 dst_sel:DWORD dst_unused:UNUSED_PAD src0_sel:WORD_1
	v_mfma_f32_32x32x16_f16 v[0:15], v[120:123], v[40:43], v[0:15]
	v_pack_b32_f16 v26, v27, v26
	v_pk_fma_f16 v134, v25, v26, v24 neg_lo:[1,0,0] neg_hi:[1,0,0]
	v_pack_b32_f16 v24, v31, v30
	v_pk_add_f16 v25, v29, v28
	v_add_co_u32_e32 v150, vcc, s6, v156
	v_pk_fma_f16 v135, v29, v24, v25 neg_lo:[1,0,0] neg_hi:[1,0,0]
	s_waitcnt vmcnt(4)
	v_mfma_f32_32x32x16_f16 v[0:15], v[16:19], v[32:35], v[0:15]
	v_addc_co_u32_e32 v151, vcc, 0, v157, vcc
	global_load_dwordx4 v[64:67], v[138:139], off
	global_load_dwordx4 v[84:87], v[138:139], off offset:2048
	s_mov_b32 s6, 0x10000
	v_add_co_u32_e32 v140, vcc, s6, v156
	s_nop 6
	v_cvt_pk_f16_f32 v16, v0, v1
	v_and_b32_e32 v17, 0x7fff7fff, v16
	v_pk_fma_f16 v0, v17, s2, v164 op_sel_hi:[1,0,0]
	v_cvt_pk_f16_f32 v24, v2, v3
	v_pk_fma_f16 v0, v0, v17, s3 op_sel_hi:[1,1,0]
	v_and_b32_e32 v25, 0x7fff7fff, v24
	v_pk_mul_f16 v0, v17, v0
	v_pk_add_f16 v16, v17, v16
	v_exp_f16_e32 v18, v0
	v_exp_f16_sdwa v19, v0 dst_sel:DWORD dst_unused:UNUSED_PAD src0_sel:WORD_1
	v_pk_fma_f16 v0, v25, s2, v164 op_sel_hi:[1,0,0]
	v_addc_co_u32_e32 v141, vcc, 0, v157, vcc
	v_pk_fma_f16 v0, v0, v25, s3 op_sel_hi:[1,1,0]
	v_pack_b32_f16 v18, v18, v19
	v_pk_mul_f16 v26, v25, v0
	global_load_dwordx4 v[0:3], v[150:151], off offset:-4096
	v_exp_f16_e32 v27, v26
	v_exp_f16_sdwa v26, v26 dst_sel:DWORD dst_unused:UNUSED_PAD src0_sel:WORD_1
	v_pk_fma_f16 v120, v17, v18, v16 neg_lo:[1,0,0] neg_hi:[1,0,0]
	v_pk_add_f16 v17, v25, v24
	global_load_dwordx4 v[88:91], v[140:141], off offset:-4096
	v_pack_b32_f16 v16, v27, v26
	v_pk_fma_f16 v121, v25, v16, v17 neg_lo:[1,0,0] neg_hi:[1,0,0]
	s_waitcnt vmcnt(6)
	v_mfma_f32_32x32x16_f16 v[16:31], v[20:23], v[96:99], 0
	v_cvt_pk_f16_f32 v82, v4, v5
	s_mov_b32 s6, 0xf000
	v_and_b32_e32 v122, 0x7fff7fff, v82
	v_add_co_u32_e32 v162, vcc, s6, v156
	v_pk_fma_f16 v4, v122, s2, v164 op_sel_hi:[1,0,0]
	s_nop 0
	v_addc_co_u32_e32 v163, vcc, 0, v157, vcc
	v_mfma_f32_32x32x16_f16 v[16:31], v[44:47], v[104:107], v[16:31]
	v_pk_fma_f16 v4, v4, v122, s3 op_sel_hi:[1,1,0]
	global_load_dwordx4 v[92:95], v[162:163], off offset:2048
	v_pk_mul_f16 v4, v122, v4
	v_cvt_pk_f16_f32 v45, v6, v7
	v_exp_f16_e32 v5, v4
	v_exp_f16_sdwa v4, v4 dst_sel:DWORD dst_unused:UNUSED_PAD src0_sel:WORD_1
	v_and_b32_e32 v46, 0x7fff7fff, v45
	s_waitcnt vmcnt(6)
	v_mfma_f32_32x32x16_f16 v[16:31], v[142:145], v[100:103], v[16:31]
	s_mov_b32 s6, 0x11000
	v_pack_b32_f16 v44, v5, v4
	v_pk_fma_f16 v4, v46, s2, v164 op_sel_hi:[1,0,0]
	v_cvt_pk_f16_f32 v10, v10, v11
	v_pk_fma_f16 v4, v4, v46, s3 op_sel_hi:[1,1,0]
	v_and_b32_e32 v11, 0x7fff7fff, v10
	v_pk_mul_f16 v47, v46, v4
	v_mfma_f32_32x32x16_f16 v[16:31], v[76:79], v[112:115], v[16:31]
	global_load_dwordx4 v[4:7], v[140:141], off
	v_exp_f16_e32 v76, v47
	v_exp_f16_sdwa v47, v47 dst_sel:DWORD dst_unused:UNUSED_PAD src0_sel:WORD_1
	v_pk_add_f16 v77, v122, v82
	v_pk_add_f16 v45, v46, v45
	v_pk_fma_f16 v122, v122, v44, v77 neg_lo:[1,0,0] neg_hi:[1,0,0]
	v_pack_b32_f16 v44, v76, v47
	v_mfma_f32_32x32x16_f16 v[16:31], v[152:155], v[108:111], v[16:31]
	global_load_dwordx4 v[76:79], v[140:141], off offset:2048
	v_cvt_pk_f16_f32 v47, v8, v9
	v_add_co_u32_e32 v8, vcc, s6, v156
	v_and_b32_e32 v82, 0x7fff7fff, v47
	s_nop 0
	v_addc_co_u32_e32 v9, vcc, 0, v157, vcc
	v_mfma_f32_32x32x16_f16 v[16:31], v[146:149], v[72:75], v[16:31]
	global_load_dwordx4 v[72:75], v[8:9], off
	v_pk_fma_f16 v123, v82, s2, v164 op_sel_hi:[1,0,0]
	s_mov_b32 s6, 0x12000
	v_pk_fma_f16 v123, v123, v82, s3 op_sel_hi:[1,1,0]
	v_add_co_u32_e32 v160, vcc, s6, v156
	global_load_dwordx4 v[146:149], v[138:139], off offset:1024
	v_mfma_f32_32x32x16_f16 v[16:31], v[166:169], v[68:71], v[16:31]
	v_pk_mul_f16 v68, v82, v123
	v_addc_co_u32_e32 v161, vcc, 0, v157, vcc
	v_exp_f16_e32 v136, v68
	v_exp_f16_sdwa v137, v68 dst_sel:DWORD dst_unused:UNUSED_PAD src0_sel:WORD_1
	global_load_dwordx4 v[68:71], v[8:9], off offset:2048
	global_load_dwordx4 v[142:145], v[160:161], off offset:1024
	s_waitcnt vmcnt(11)
	v_mfma_f32_32x32x16_f16 v[16:31], v[170:173], v[40:43], v[16:31]
	v_pk_fma_f16 v123, v46, v44, v45 neg_lo:[1,0,0] neg_hi:[1,0,0]
	v_pack_b32_f16 v136, v136, v137
	v_pk_add_f16 v137, v82, v47
	global_load_dwordx4 v[170:173], v[140:141], off offset:3072
	v_pk_fma_f16 v136, v82, v136, v137 neg_lo:[1,0,0] neg_hi:[1,0,0]
	s_mov_b32 s6, 0x16000
	global_load_dwordx4 v[152:155], v[150:151], off
	v_mfma_f32_32x32x16_f16 v[16:31], v[36:39], v[32:35], v[16:31]
	v_pk_fma_f16 v32, v11, s2, v164 op_sel_hi:[1,0,0]
	s_nop 0
	v_pk_fma_f16 v32, v32, v11, s3 op_sel_hi:[1,1,0]
	s_nop 0
	v_pk_mul_f16 v32, v11, v32
	s_nop 6
	v_cvt_pk_f16_f32 v24, v24, v25
	v_exp_f16_e32 v165, v32
	v_exp_f16_sdwa v166, v32 dst_sel:DWORD dst_unused:UNUSED_PAD src0_sel:WORD_1
	s_waitcnt vmcnt(10)
	v_mfma_f32_32x32x16_f16 v[32:47], v[0:3], v[96:99], 0
	v_pk_add_f16 v1, v11, v10
	v_cvt_pk_f16_f32 v10, v14, v15
	v_pack_b32_f16 v0, v165, v166
	global_load_dwordx4 v[166:169], v[138:139], off offset:3072
	v_pk_fma_f16 v137, v11, v0, v1 neg_lo:[1,0,0] neg_hi:[1,0,0]
	v_cvt_pk_f16_f32 v0, v12, v13
	v_and_b32_e32 v1, 0x7fff7fff, v0
	v_mfma_f32_32x32x16_f16 v[32:47], v[64:67], v[104:107], v[32:47]
	global_load_dwordx4 v[64:67], v[162:163], off offset:1024
	v_pk_fma_f16 v2, v1, s2, v164 op_sel_hi:[1,0,0]
	v_and_b32_e32 v11, 0x7fff7fff, v10
	v_pk_fma_f16 v2, v2, v1, s3 op_sel_hi:[1,1,0]
	v_pk_fma_f16 v12, v11, s2, v164 op_sel_hi:[1,0,0]
	v_pk_mul_f16 v2, v1, v2
	v_pk_fma_f16 v12, v12, v11, s3 op_sel_hi:[1,1,0]
	v_mfma_f32_32x32x16_f16 v[32:47], v[84:87], v[100:103], v[32:47]
	v_exp_f16_e32 v3, v2
	v_exp_f16_sdwa v2, v2 dst_sel:DWORD dst_unused:UNUSED_PAD src0_sel:WORD_1
	v_pk_mul_f16 v12, v11, v12
	v_pk_add_f16 v0, v1, v0
	v_exp_f16_e32 v13, v12
	v_exp_f16_sdwa v12, v12 dst_sel:DWORD dst_unused:UNUSED_PAD src0_sel:WORD_1
	v_pack_b32_f16 v2, v3, v2
	s_waitcnt vmcnt(11)
	v_mfma_f32_32x32x16_f16 v[32:47], v[88:91], v[112:115], v[32:47]
	global_load_dwordx4 v[88:91], v[162:163], off offset:3072
	v_pk_fma_f16 v138, v1, v2, v0 neg_lo:[1,0,0] neg_hi:[1,0,0]
	v_pack_b32_f16 v0, v13, v12
	v_pk_add_f16 v1, v11, v10
	v_add_co_u32_e32 v162, vcc, s6, v156
	v_pk_fma_f16 v139, v11, v0, v1 neg_lo:[1,0,0] neg_hi:[1,0,0]
	s_waitcnt vmcnt(11)
	v_mfma_f32_32x32x16_f16 v[32:47], v[92:95], v[108:111], v[32:47]
	global_load_dwordx4 v[92:95], v[140:141], off offset:1024
	v_cvt_pk_f16_f32 v0, v16, v17
	v_and_b32_e32 v1, 0x7fff7fff, v0
	v_pk_fma_f16 v2, v1, s2, v164 op_sel_hi:[1,0,0]
	v_pk_add_f16 v0, v1, v0
	v_pk_fma_f16 v2, v2, v1, s3 op_sel_hi:[1,1,0]
	v_addc_co_u32_e32 v163, vcc, 0, v157, vcc
	s_waitcnt vmcnt(11)
	v_mfma_f32_32x32x16_f16 v[32:47], v[4:7], v[48:51], v[32:47]
	v_cvt_pk_f16_f32 v4, v18, v19
	v_and_b32_e32 v5, 0x7fff7fff, v4
	global_load_dwordx4 v[16:19], v[8:9], off offset:1024
	v_pk_fma_f16 v6, v5, s2, v164 op_sel_hi:[1,0,0]
	v_pk_mul_f16 v2, v1, v2
	v_pk_fma_f16 v6, v6, v5, s3 op_sel_hi:[1,1,0]
	v_exp_f16_e32 v3, v2
	s_waitcnt vmcnt(11)
	v_mfma_f32_32x32x16_f16 v[32:47], v[76:79], v[52:55], v[32:47]
	v_exp_f16_sdwa v2, v2 dst_sel:DWORD dst_unused:UNUSED_PAD src0_sel:WORD_1
	v_pk_mul_f16 v6, v5, v6
	global_load_dwordx4 v[84:87], v[150:151], off offset:3072
	v_exp_f16_e32 v7, v6
	v_exp_f16_sdwa v6, v6 dst_sel:DWORD dst_unused:UNUSED_PAD src0_sel:WORD_1
	v_pack_b32_f16 v2, v3, v2
	v_pk_fma_f16 v140, v1, v2, v0 neg_lo:[1,0,0] neg_hi:[1,0,0]
	s_waitcnt vmcnt(11)
	v_mfma_f32_32x32x16_f16 v[32:47], v[72:75], v[56:59], v[32:47]
	v_pack_b32_f16 v0, v7, v6
	global_load_dwordx4 v[72:75], v[8:9], off offset:3072
	v_pk_add_f16 v1, v5, v4
	s_mov_b32 s6, 0x14000
	v_pk_fma_f16 v141, v5, v0, v1 neg_lo:[1,0,0] neg_hi:[1,0,0]
	v_lshlrev_b32_e32 v0, 2, v159
	v_ashrrev_i32_e32 v1, 31, v0
	v_lshl_add_u64 v[0:1], v[0:1], 2, v[80:81]
	global_load_dwordx4 v[76:79], v[0:1], off
	s_waitcnt vmcnt(11)
	v_mfma_f32_32x32x16_f16 v[32:47], v[68:71], v[60:63], v[32:47]
	global_load_dwordx4 v[68:71], v[162:163], off offset:2048
	global_load_dwordx4 v[174:177], v[160:161], off offset:2048
	s_waitcnt vmcnt(2)
	v_cvt_pk_f16_f32 v79, v20, v21
	v_and_b32_e32 v80, 0x7fff7fff, v79
	v_pk_fma_f16 v20, v80, s2, v164 op_sel_hi:[1,0,0]
	v_pk_add_f16 v79, v80, v79
	v_pk_fma_f16 v20, v20, v80, s3 op_sel_hi:[1,1,0]
	v_and_b32_e32 v25, 0x7fff7fff, v24
	v_mfma_f32_32x32x16_f16 v[0:15], v[142:145], v[96:99], 0
	v_cvt_pk_f16_f32 v143, v22, v23
	v_pk_mul_f16 v20, v80, v20
	v_and_b32_e32 v144, 0x7fff7fff, v143
	v_exp_f16_e32 v81, v20
	v_exp_f16_sdwa v82, v20 dst_sel:DWORD dst_unused:UNUSED_PAD src0_sel:WORD_1
	v_pk_fma_f16 v20, v144, s2, v164 op_sel_hi:[1,0,0]
	v_cvt_pk_f16_f32 v26, v26, v27
	v_pk_fma_f16 v20, v20, v144, s3 op_sel_hi:[1,1,0]
	v_mfma_f32_32x32x16_f16 v[0:15], v[146:149], v[104:107], v[0:15]
	v_pk_mul_f16 v142, v144, v20
	global_load_dwordx4 v[20:23], v[150:151], off offset:2048
	v_add_co_u32_e32 v148, vcc, s6, v156
	s_mov_b32 s6, 0x15000
	s_nop 0
	v_addc_co_u32_e32 v149, vcc, 0, v157, vcc
	v_mfma_f32_32x32x16_f16 v[0:15], v[166:169], v[100:103], v[0:15]
	global_load_dwordx4 v[166:169], v[148:149], off offset:2048
	global_load_dwordx4 v[178:181], v[160:161], off offset:3072
	v_add_co_u32_e32 v194, vcc, s6, v156
	v_exp_f16_e32 v145, v142
	s_nop 0
	v_addc_co_u32_e32 v195, vcc, 0, v157, vcc
	v_exp_f16_sdwa v146, v142 dst_sel:DWORD dst_unused:UNUSED_PAD src0_sel:WORD_1
	v_mfma_f32_32x32x16_f16 v[0:15], v[64:67], v[112:115], v[0:15]
	global_load_dwordx4 v[64:67], v[194:195], off offset:2048
	v_pack_b32_f16 v81, v81, v82
	v_pk_fma_f16 v142, v80, v81, v79 neg_lo:[1,0,0] neg_hi:[1,0,0]
	v_pack_b32_f16 v79, v145, v146
	v_pk_add_f16 v80, v144, v143
	s_mov_b32 s6, 0x18000
	v_pk_fma_f16 v143, v144, v79, v80 neg_lo:[1,0,0] neg_hi:[1,0,0]
	v_mfma_f32_32x32x16_f16 v[0:15], v[88:91], v[108:111], v[0:15]
	global_load_dwordx4 v[88:91], v[162:163], off offset:3072
	v_pk_fma_f16 v79, v25, s2, v164 op_sel_hi:[1,0,0]
	v_add_co_u32_e32 v160, vcc, s6, v156
	v_pk_fma_f16 v79, v79, v25, s3 op_sel_hi:[1,1,0]
	v_pk_add_f16 v24, v25, v24
	v_pk_mul_f16 v79, v25, v79
	v_mfma_f32_32x32x16_f16 v[0:15], v[92:95], v[48:51], v[0:15]
	global_load_dwordx4 v[92:95], v[148:149], off offset:3072
	global_load_dwordx4 v[186:189], v[148:149], off offset:1024
	v_exp_f16_e32 v48, v79
	v_exp_f16_sdwa v49, v79 dst_sel:DWORD dst_unused:UNUSED_PAD src0_sel:WORD_1
	v_addc_co_u32_e32 v161, vcc, 0, v157, vcc
	v_and_b32_e32 v27, 0x7fff7fff, v26
	v_mfma_f32_32x32x16_f16 v[0:15], v[170:173], v[52:55], v[0:15]
	v_pack_b32_f16 v48, v48, v49
	v_pk_fma_f16 v144, v25, v48, v24 neg_lo:[1,0,0] neg_hi:[1,0,0]
	v_cvt_pk_f16_f32 v25, v28, v29
	v_pk_fma_f16 v50, v27, s2, v164 op_sel_hi:[1,0,0]
	v_mov_b32_e32 v82, v83
	v_pk_fma_f16 v50, v50, v27, s3 op_sel_hi:[1,1,0]
	global_load_dwordx4 v[170:173], v[194:195], off offset:-4096
	v_mfma_f32_32x32x16_f16 v[0:15], v[16:19], v[56:59], v[0:15]
	v_pk_mul_f16 v50, v27, v50
	global_load_dwordx4 v[182:185], v[194:195], off
	v_exp_f16_e32 v51, v50
	v_exp_f16_sdwa v50, v50 dst_sel:DWORD dst_unused:UNUSED_PAD src0_sel:WORD_1
	v_and_b32_e32 v16, 0x7fff7fff, v25
	v_pk_fma_f16 v17, v16, s2, v164 op_sel_hi:[1,0,0]
	s_mov_b32 s6, 0x17000
	v_mfma_f32_32x32x16_f16 v[0:15], v[72:75], v[60:63], v[0:15]
	global_load_dwordx4 v[72:75], v[194:195], off offset:3072
	v_pack_b32_f16 v24, v51, v50
	v_cvt_pk_f16_f32 v19, v76, v77
	v_cvt_pk_f16_f32 v28, v78, 1.0
	global_load_dwordx4 v[76:79], v[160:161], off offset:-4096
	v_cndmask_b32_e64 v80, 0, v19, s[4:5]
	v_cndmask_b32_e64 v81, 0, v28, s[4:5]
	v_pk_fma_f16 v17, v17, v16, s3 op_sel_hi:[1,1,0]
	v_add_co_u32_e32 v202, vcc, s6, v156
	s_waitcnt vmcnt(12)
	v_mfma_f32_32x32x16_f16 v[48:63], v[68:71], v[80:83], 0
	v_pk_mul_f16 v17, v16, v17
	v_addc_co_u32_e32 v203, vcc, 0, v157, vcc
	v_exp_f16_e32 v18, v17
	v_exp_f16_sdwa v17, v17 dst_sel:DWORD dst_unused:UNUSED_PAD src0_sel:WORD_1
	global_load_dwordx4 v[190:193], v[202:203], off offset:1024
	v_pk_add_f16 v19, v27, v26
	s_waitcnt vmcnt(12)
	v_mfma_f32_32x32x16_f16 v[48:63], v[174:177], v[116:119], v[48:63]
	v_pk_fma_f16 v145, v27, v24, v19 neg_lo:[1,0,0] neg_hi:[1,0,0]
	v_pack_b32_f16 v17, v18, v17
	v_pk_add_f16 v18, v16, v25
	v_cvt_pk_f16_f32 v19, v30, v31
	v_and_b32_e32 v24, 0x7fff7fff, v19
	v_pk_fma_f16 v146, v16, v17, v18 neg_lo:[1,0,0] neg_hi:[1,0,0]
	v_cvt_pk_f16_f32 v17, v32, v33
	s_waitcnt vmcnt(11)
	v_mfma_f32_32x32x16_f16 v[48:63], v[20:23], v[124:127], v[48:63]
	v_pk_fma_f16 v25, v24, s2, v164 op_sel_hi:[1,0,0]
	v_and_b32_e32 v32, 0x7fff7fff, v17
	v_pk_fma_f16 v25, v25, v24, s3 op_sel_hi:[1,1,0]
	v_pk_fma_f16 v18, v32, s2, v164 op_sel_hi:[1,0,0]
	v_pk_mul_f16 v25, v24, v25
	v_pk_fma_f16 v18, v18, v32, s3 op_sel_hi:[1,1,0]
	v_exp_f16_e32 v26, v25
	s_waitcnt vmcnt(10)
	v_mfma_f32_32x32x16_f16 v[48:63], v[166:169], v[128:131], v[48:63]
	global_load_dwordx4 v[166:169], v[162:163], off
	v_exp_f16_sdwa v25, v25 dst_sel:DWORD dst_unused:UNUSED_PAD src0_sel:WORD_1
	global_load_dwordx4 v[174:177], v[150:151], off offset:1024
	v_pk_mul_f16 v18, v32, v18
	v_pk_add_f16 v19, v24, v19
	v_exp_f16_e32 v20, v18
	v_exp_f16_sdwa v18, v18 dst_sel:DWORD dst_unused:UNUSED_PAD src0_sel:WORD_1
	v_pack_b32_f16 v16, v26, v25
	v_pk_fma_f16 v147, v24, v16, v19 neg_lo:[1,0,0] neg_hi:[1,0,0]
	s_waitcnt vmcnt(10)
	v_mfma_f32_32x32x16_f16 v[48:63], v[64:67], v[132:135], v[48:63]
	v_pack_b32_f16 v33, v20, v18
	v_pk_add_f16 v64, v32, v17
	v_cvt_pk_f16_f32 v36, v36, v37
	v_pk_fma_f16 v148, v32, v33, v64 neg_lo:[1,0,0] neg_hi:[1,0,0]
	v_cvt_pk_f16_f32 v32, v34, v35
	v_and_b32_e32 v33, 0x7fff7fff, v32
	v_pk_fma_f16 v34, v33, s2, v164 op_sel_hi:[1,0,0]
	s_waitcnt vmcnt(9)
	v_mfma_f32_32x32x16_f16 v[16:31], v[88:91], v[80:83], 0
	v_pk_fma_f16 v34, v34, v33, s3 op_sel_hi:[1,1,0]
	v_and_b32_e32 v37, 0x7fff7fff, v36
	v_pk_mul_f16 v34, v33, v34
	v_pk_add_f16 v32, v33, v32
	v_exp_f16_e32 v35, v34
	v_exp_f16_sdwa v34, v34 dst_sel:DWORD dst_unused:UNUSED_PAD src0_sel:WORD_1
	v_pk_fma_f16 v64, v37, s2, v164 op_sel_hi:[1,0,0]
	v_mfma_f32_32x32x16_f16 v[16:31], v[178:181], v[116:119], v[16:31]
	v_pk_fma_f16 v64, v64, v37, s3 op_sel_hi:[1,1,0]
	v_pack_b32_f16 v34, v35, v34
	v_pk_fma_f16 v149, v33, v34, v32 neg_lo:[1,0,0] neg_hi:[1,0,0]
	global_load_dwordx4 v[32:35], v[194:195], off offset:1024
	v_pk_mul_f16 v64, v37, v64
	v_pk_add_f16 v36, v37, v36
	v_exp_f16_e32 v65, v64
	v_exp_f16_sdwa v64, v64 dst_sel:DWORD dst_unused:UNUSED_PAD src0_sel:WORD_1
	v_mfma_f32_32x32x16_f16 v[16:31], v[84:87], v[124:127], v[16:31]
	v_cvt_pk_f16_f32 v84, v38, v39
	v_and_b32_e32 v85, 0x7fff7fff, v84
	v_pack_b32_f16 v64, v65, v64
	v_pk_fma_f16 v150, v37, v64, v36 neg_lo:[1,0,0] neg_hi:[1,0,0]
	v_pk_fma_f16 v36, v85, s2, v164 op_sel_hi:[1,0,0]
	s_mov_b32 s6, 0x1b000
	v_pk_fma_f16 v64, v36, v85, s3 op_sel_hi:[1,1,0]
	global_load_dwordx4 v[36:39], v[162:163], off offset:1024
	s_waitcnt vmcnt(10)
	v_mfma_f32_32x32x16_f16 v[16:31], v[92:95], v[128:131], v[16:31]
	v_add_co_u32_e32 v204, vcc, s6, v156
	v_pk_mul_f16 v86, v85, v64
	s_nop 0
	v_addc_co_u32_e32 v205, vcc, 0, v157, vcc
	global_load_dwordx4 v[178:181], v[204:205], off offset:2048
	global_load_dwordx4 v[194:197], v[160:161], off
	global_load_dwordx4 v[198:201], v[202:203], off offset:2048
	s_waitcnt vmcnt(9)
	v_mfma_f32_32x32x16_f16 v[16:31], v[72:75], v[132:135], v[16:31]
	v_cvt_pk_f16_f32 v40, v40, v41
	v_and_b32_e32 v41, 0x7fff7fff, v40
	v_pk_fma_f16 v88, v41, s2, v164 op_sel_hi:[1,0,0]
	v_exp_f16_e32 v87, v86
	v_pk_fma_f16 v88, v88, v41, s3 op_sel_hi:[1,1,0]
	v_exp_f16_sdwa v86, v86 dst_sel:DWORD dst_unused:UNUSED_PAD src0_sel:WORD_1
	v_pk_mul_f16 v88, v41, v88
	s_waitcnt vmcnt(8)
	v_mfma_f32_32x32x16_f16 v[64:79], v[76:79], v[80:83], 0
	v_exp_f16_e32 v89, v88
	v_exp_f16_sdwa v88, v88 dst_sel:DWORD dst_unused:UNUSED_PAD src0_sel:WORD_1
	v_pack_b32_f16 v86, v87, v86
	v_pk_add_f16 v84, v85, v84
	v_pk_add_f16 v40, v41, v40
	v_pk_fma_f16 v151, v85, v86, v84 neg_lo:[1,0,0] neg_hi:[1,0,0]
	v_pack_b32_f16 v84, v89, v88
	v_mfma_f32_32x32x16_f16 v[64:79], v[152:155], v[116:119], v[64:79]
	v_pk_fma_f16 v152, v41, v84, v40 neg_lo:[1,0,0] neg_hi:[1,0,0]
	v_cvt_pk_f16_f32 v153, v42, v43
	global_load_dwordx4 v[40:43], v[160:161], off offset:2048
	s_mov_b32 s6, 0x1a000
	v_add_co_u32_e32 v154, vcc, s6, v156
	s_mov_b32 s6, 0x19000
	v_mfma_f32_32x32x16_f16 v[64:79], v[170:173], v[124:127], v[64:79]
	v_addc_co_u32_e32 v155, vcc, 0, v157, vcc
	global_load_dwordx4 v[170:173], v[154:155], off offset:-4096
	v_add_co_u32_e32 v162, vcc, s6, v156
	v_and_b32_e32 v159, 0x7fff7fff, v153
	s_nop 0
	v_addc_co_u32_e32 v163, vcc, 0, v157, vcc
	v_mfma_f32_32x32x16_f16 v[64:79], v[182:185], v[128:131], v[64:79]
	v_pk_fma_f16 v84, v159, s2, v164 op_sel_hi:[1,0,0]
	global_load_dwordx4 v[182:185], v[154:155], off
	v_pk_fma_f16 v84, v84, v159, s3 op_sel_hi:[1,1,0]
	s_mov_b32 s6, 0x1c000
	v_pk_mul_f16 v84, v159, v84
	v_cvt_pk_f16_f32 v48, v48, v49
	v_exp_f16_e32 v165, v84
	s_waitcnt vmcnt(9)
	v_mfma_f32_32x32x16_f16 v[64:79], v[166:169], v[132:135], v[64:79]
	global_load_dwordx4 v[166:169], v[162:163], off offset:2048
	v_exp_f16_sdwa v206, v84 dst_sel:DWORD dst_unused:UNUSED_PAD src0_sel:WORD_1
	v_cvt_pk_f16_f32 v49, v50, v51
	v_cvt_pk_f16_f32 v50, v52, v53
	v_cvt_pk_f16_f32 v51, v54, v55
	v_cvt_pk_f16_f32 v24, v24, v25
	v_cvt_pk_f16_f32 v25, v26, v27
	v_mfma_f32_32x32x16_f16 v[80:95], v[190:193], v[80:83], 0
	v_cvt_pk_f16_f32 v26, v28, v29
	v_cvt_pk_f16_f32 v27, v30, v31
	global_load_dwordx4 v[28:31], v[160:161], off offset:3072
	v_cvt_pk_f16_f32 v20, v20, v21
	v_cvt_pk_f16_f32 v21, v22, v23
	v_pk_max_f16 v23, v21, 0
	v_pk_max_f16 v22, v20, 0
	s_waitcnt vmcnt(10)
	v_mfma_f32_32x32x16_f16 v[80:95], v[174:177], v[116:119], v[80:95]
	global_load_dwordx4 v[116:119], v[154:155], off offset:2048
	v_pk_max_f16 v176, v50, 0
	v_pk_max_f16 v175, v49, 0
	v_pk_max_f16 v174, v48, 0
	v_cvt_pk_f16_f32 v48, v56, v57
	v_cvt_pk_f16_f32 v49, v58, v59
	v_cvt_pk_f16_f32 v50, v60, v61
	v_mfma_f32_32x32x16_f16 v[80:95], v[186:189], v[124:127], v[80:95]
	v_add_co_u32_e32 v186, vcc, s6, v156
	v_pk_max_f16 v177, v51, 0
	s_nop 0
	v_addc_co_u32_e32 v187, vcc, 0, v157, vcc
	global_load_dwordx4 v[124:127], v[186:187], off offset:-4096
	v_pk_max_f16 v27, v27, 0
	s_waitcnt vmcnt(11)
	v_mfma_f32_32x32x16_f16 v[80:95], v[32:35], v[128:131], v[80:95]
	v_cvt_pk_f16_f32 v32, v62, v63
	v_pk_max_f16 v131, v32, 0
	global_load_dwordx4 v[32:35], v[204:205], off offset:3072
	v_pk_max_f16 v130, v50, 0
	v_pk_max_f16 v129, v49, 0
	v_pk_max_f16 v128, v48, 0
	v_pk_max_f16 v26, v26, 0
	s_waitcnt vmcnt(11)
	v_mfma_f32_32x32x16_f16 v[80:95], v[36:39], v[132:135], v[80:95]
	v_cvt_pk_f16_f32 v36, v16, v17
	v_cvt_pk_f16_f32 v37, v18, v19
	global_load_dwordx4 v[16:19], v[202:203], off offset:3072
	global_load_dwordx4 v[132:135], v[160:161], off offset:1024
	v_cvt_pk_f16_f32 v38, v68, v69
	v_cvt_pk_f16_f32 v39, v70, v71
	global_load_dwordx4 v[68:71], v[162:163], off offset:1024
	s_waitcnt vmcnt(13)
	v_mfma_f32_32x32x16_f16 v[48:63], v[178:181], v[96:99], 0
	v_pk_max_f16 v21, v37, 0
	v_pk_max_f16 v20, v36, 0
	v_cvt_pk_f16_f32 v36, v64, v65
	v_cvt_pk_f16_f32 v37, v66, v67
	v_pk_max_f16 v65, v37, 0
	v_pk_max_f16 v64, v36, 0
	v_cvt_pk_f16_f32 v36, v72, v73
	s_waitcnt vmcnt(11)
	v_mfma_f32_32x32x16_f16 v[48:63], v[198:201], v[174:177], v[48:63]
	v_cvt_pk_f16_f32 v37, v74, v75
	global_load_dwordx4 v[72:75], v[162:163], off offset:3072
	v_pk_max_f16 v25, v25, 0
	v_pk_max_f16 v24, v24, 0
	v_pk_max_f16 v67, v39, 0
	v_pk_max_f16 v66, v38, 0
	global_load_dwordx4 v[160:163], v[154:155], off offset:1024
	v_mfma_f32_32x32x16_f16 v[48:63], v[194:197], v[128:131], v[48:63]
	v_cvt_pk_f16_f32 v38, v76, v77
	v_cvt_pk_f16_f32 v39, v78, v79
	v_pk_max_f16 v79, v39, 0
	v_pk_max_f16 v78, v38, 0
	v_pk_max_f16 v77, v37, 0
	v_pk_max_f16 v76, v36, 0
	v_cvt_pk_f16_f32 v36, v80, v81
	s_waitcnt vmcnt(12)
	v_mfma_f32_32x32x16_f16 v[48:63], v[40:43], v[20:23], v[48:63]
	v_cvt_pk_f16_f32 v38, v84, v85
	v_cvt_pk_f16_f32 v39, v86, v87
	global_load_dwordx4 v[84:87], v[154:155], off offset:3072
	v_cvt_pk_f16_f32 v37, v82, v83
	v_pk_max_f16 v80, v36, 0
	v_cvt_pk_f16_f32 v36, v92, v93
	s_mov_b32 s6, 0x20000
	s_waitcnt vmcnt(12)
	v_mfma_f32_32x32x16_f16 v[48:63], v[170:173], v[24:27], v[48:63]
	v_pk_max_f16 v83, v39, 0
	v_pk_max_f16 v81, v37, 0
	v_cvt_pk_f16_f32 v39, v90, v91
	v_cvt_pk_f16_f32 v37, v94, v95
	v_pk_max_f16 v90, v36, 0
	v_add_co_u32_e32 v36, vcc, s6, v156
	s_waitcnt vmcnt(10)
	v_mfma_f32_32x32x16_f16 v[48:63], v[166:169], v[64:67], v[48:63]
	v_pk_max_f16 v82, v38, 0
	v_pk_max_f16 v91, v37, 0
	v_addc_co_u32_e32 v37, vcc, 0, v157, vcc
	global_load_dwordx4 v[92:95], v[204:205], off offset:1024
	v_cvt_pk_f16_f32 v207, v44, v45
	v_and_b32_e32 v190, 0x7fff7fff, v207
	v_mfma_f32_32x32x16_f16 v[48:63], v[182:185], v[76:79], v[48:63]
	global_load_dwordx4 v[166:169], v[186:187], off
	v_pk_fma_f16 v44, v190, s2, v164 op_sel_hi:[1,0,0]
	v_cvt_pk_f16_f32 v38, v88, v89
	v_pk_fma_f16 v44, v44, v190, s3 op_sel_hi:[1,1,0]
	v_pk_max_f16 v88, v38, 0
	v_pk_mul_f16 v44, v190, v44
	v_pk_add_f16 v38, v159, v153
	s_waitcnt vmcnt(10)
	v_mfma_f32_32x32x16_f16 v[48:63], v[116:119], v[80:83], v[48:63]
	global_load_dwordx4 v[116:119], v[36:37], off
	v_exp_f16_e32 v45, v44
	v_exp_f16_sdwa v36, v44 dst_sel:DWORD dst_unused:UNUSED_PAD src0_sel:WORD_1
	v_pack_b32_f16 v37, v165, v206
	v_cvt_pk_f16_f32 v155, v46, v47
	v_pk_max_f16 v89, v39, 0
	v_pk_fma_f16 v153, v159, v37, v38 neg_lo:[1,0,0] neg_hi:[1,0,0]
	v_and_b32_e32 v159, 0x7fff7fff, v155
	s_waitcnt vmcnt(10)
	v_mfma_f32_32x32x16_f16 v[48:63], v[124:127], v[88:91], v[48:63]
	v_pk_fma_f16 v124, v159, s2, v164 op_sel_hi:[1,0,0]
	v_pack_b32_f16 v154, v45, v36
	v_pk_fma_f16 v124, v124, v159, s3 op_sel_hi:[1,1,0]
	v_pk_add_f16 v171, v190, v207
	v_pk_mul_f16 v165, v159, v124
	global_load_dwordx4 v[124:127], v[186:187], off offset:1024
	v_exp_f16_e32 v170, v165
	s_waitcnt vmcnt(10)
	v_mfma_f32_32x32x16_f16 v[32:47], v[32:35], v[96:99], 0
	v_exp_f16_sdwa v165, v165 dst_sel:DWORD dst_unused:UNUSED_PAD src0_sel:WORD_1
	v_pk_fma_f16 v154, v190, v154, v171 neg_lo:[1,0,0] neg_hi:[1,0,0]
	s_mov_b32 s6, 0x1e000
	v_cvt_pk_f16_f32 v4, v4, v5
	v_and_b32_e32 v5, 0x7fff7fff, v4
	v_cvt_pk_f16_f32 v56, v56, v57
	v_cvt_pk_f16_f32 v57, v58, v59
	s_waitcnt vmcnt(9)
	v_mfma_f32_32x32x16_f16 v[32:47], v[16:19], v[174:177], v[32:47]
	v_pack_b32_f16 v16, v170, v165
	global_load_dwordx4 v[170:173], v[186:187], off offset:2048
	v_add_co_u32_e32 v174, vcc, s6, v156
	v_cvt_pk_f16_f32 v18, v0, v1
	s_nop 0
	v_addc_co_u32_e32 v175, vcc, 0, v157, vcc
	s_waitcnt vmcnt(9)
	v_mfma_f32_32x32x16_f16 v[32:47], v[132:135], v[128:131], v[32:47]
	global_load_dwordx4 v[128:131], v[186:187], off offset:3072
	v_and_b32_e32 v19, 0x7fff7fff, v18
	global_load_dwordx4 v[132:135], v[174:175], off offset:-4096
	v_pk_fma_f16 v0, v19, s2, v164 op_sel_hi:[1,0,0]
	v_pk_add_f16 v17, v159, v155
	v_pk_fma_f16 v0, v0, v19, s3 op_sel_hi:[1,1,0]
	s_mov_b32 s6, 0x1d000
	v_mfma_f32_32x32x16_f16 v[32:47], v[28:31], v[20:23], v[32:47]
	v_pk_mul_f16 v0, v19, v0
	v_pk_fma_f16 v155, v159, v16, v17 neg_lo:[1,0,0] neg_hi:[1,0,0]
	v_exp_f16_e32 v1, v0
	v_exp_f16_sdwa v0, v0 dst_sel:DWORD dst_unused:UNUSED_PAD src0_sel:WORD_1
	v_add_co_u32_e32 v16, vcc, s6, v156
	v_cvt_pk_f16_f32 v20, v2, v3
	s_nop 0
	v_addc_co_u32_e32 v17, vcc, 0, v157, vcc
	v_pack_b32_f16 v159, v1, v0
	s_waitcnt vmcnt(10)
	v_mfma_f32_32x32x16_f16 v[32:47], v[68:71], v[24:27], v[32:47]
	global_load_dwordx4 v[0:3], v[16:17], off offset:1024
	v_and_b32_e32 v21, 0x7fff7fff, v20
	v_pk_fma_f16 v22, v21, s2, v164 op_sel_hi:[1,0,0]
	v_pk_add_f16 v18, v19, v18
	v_pk_fma_f16 v22, v22, v21, s3 op_sel_hi:[1,1,0]
	v_pk_fma_f16 v68, v19, v159, v18 neg_lo:[1,0,0] neg_hi:[1,0,0]
	v_pk_mul_f16 v22, v21, v22
	s_waitcnt vmcnt(10)
	v_mfma_f32_32x32x16_f16 v[32:47], v[72:75], v[64:67], v[32:47]
	global_load_dwordx4 v[64:67], v[16:17], off offset:2048
	global_load_dwordx4 v[72:75], v[16:17], off offset:3072
	v_pk_fma_f16 v16, v5, s2, v164 op_sel_hi:[1,0,0]
	v_cvt_pk_f16_f32 v17, v50, v51
	v_pk_fma_f16 v70, v16, v5, s3 op_sel_hi:[1,1,0]
	v_cvt_pk_f16_f32 v16, v48, v49
	global_load_dwordx4 v[48:51], v[174:175], off
	s_waitcnt vmcnt(12)
	v_mfma_f32_32x32x16_f16 v[32:47], v[160:163], v[76:79], v[32:47]
	v_exp_f16_e32 v23, v22
	v_exp_f16_sdwa v22, v22 dst_sel:DWORD dst_unused:UNUSED_PAD src0_sel:WORD_1
	global_load_dwordx4 v[76:79], v[174:175], off offset:1024
	v_pk_add_f16 v19, v21, v20
	v_cvt_pk_f16_f32 v58, v60, v61
	v_pack_b32_f16 v18, v23, v22
	v_pk_fma_f16 v69, v21, v18, v19 neg_lo:[1,0,0] neg_hi:[1,0,0]
	s_waitcnt vmcnt(12)
	v_mfma_f32_32x32x16_f16 v[32:47], v[84:87], v[80:83], v[32:47]
	v_cvt_pk_f16_f32 v18, v52, v53
	v_cvt_pk_f16_f32 v19, v54, v55
	v_pk_max_f16 v55, v19, 0
	v_pk_max_f16 v54, v18, 0
	v_pk_max_f16 v53, v17, 0
	v_pk_max_f16 v52, v16, 0
	v_cvt_pk_f16_f32 v59, v62, v63
	s_waitcnt vmcnt(9)
	v_mfma_f32_32x32x16_f16 v[16:31], v[116:119], v[96:99], 0
	global_load_dwordx4 v[60:63], v[174:175], off offset:2048
	v_pk_max_f16 v59, v59, 0
	v_pk_max_f16 v58, v58, 0
	v_pk_max_f16 v57, v57, 0
	v_pk_max_f16 v56, v56, 0
	v_cvt_pk_f16_f32 v6, v6, v7
	v_and_b32_e32 v7, 0x7fff7fff, v6
	v_mfma_f32_32x32x16_f16 v[32:47], v[92:95], v[88:91], v[32:47]
	v_pk_add_f16 v4, v5, v4
	s_mov_b32 s6, 0x1f000
	v_mfma_f32_32x32x16_f16 v[16:31], v[166:169], v[52:55], v[16:31]
	s_nop 8
	v_cvt_pk_f16_f32 v32, v32, v33
	v_cvt_pk_f16_f32 v33, v34, v35
	v_cvt_pk_f16_f32 v34, v36, v37
	v_cvt_pk_f16_f32 v35, v38, v39
	global_load_dwordx4 v[36:39], v[174:175], off offset:3072
	v_pk_max_f16 v35, v35, 0
	v_pk_max_f16 v34, v34, 0
	s_waitcnt vmcnt(10)
	v_mfma_f32_32x32x16_f16 v[16:31], v[124:127], v[56:59], v[16:31]
	v_pk_max_f16 v33, v33, 0
	v_pk_max_f16 v32, v32, 0
	v_cvt_pk_f16_f32 v40, v40, v41
	v_add_co_u32_e32 v56, vcc, s6, v156
	s_nop 1
	v_addc_co_u32_e32 v57, vcc, 0, v157, vcc
	s_waitcnt vmcnt(9)
	v_mfma_f32_32x32x16_f16 v[16:31], v[170:173], v[32:35], v[16:31]
	v_cvt_pk_f16_f32 v32, v42, v43
	v_cvt_pk_f16_f32 v33, v44, v45
	v_cvt_pk_f16_f32 v34, v46, v47
	v_pk_max_f16 v35, v34, 0
	v_pk_max_f16 v34, v33, 0
	v_pk_max_f16 v33, v32, 0
	v_pk_max_f16 v32, v40, 0
	global_load_dwordx4 v[52:55], v[56:57], off
	s_waitcnt vmcnt(9)
	v_mfma_f32_32x32x16_f16 v[16:31], v[128:131], v[32:35], v[16:31]
	v_pk_fma_f16 v34, v7, s2, v164 op_sel_hi:[1,0,0]
	v_pk_mul_f16 v32, v5, v70
	v_pk_fma_f16 v34, v34, v7, s3 op_sel_hi:[1,1,0]
	v_exp_f16_e32 v33, v32
	v_exp_f16_sdwa v32, v32 dst_sel:DWORD dst_unused:UNUSED_PAD src0_sel:WORD_1
	v_pk_mul_f16 v34, v7, v34
	v_pack_b32_f16 v32, v33, v32
	s_waitcnt vmcnt(8)
	v_mfma_f32_32x32x16_f16 v[16:31], v[132:135], v[120:123], v[16:31]
	v_exp_f16_e32 v35, v34
	v_exp_f16_sdwa v34, v34 dst_sel:DWORD dst_unused:UNUSED_PAD src0_sel:WORD_1
	v_pk_fma_f16 v70, v5, v32, v4 neg_lo:[1,0,0] neg_hi:[1,0,0]
	v_pack_b32_f16 v4, v35, v34
	s_waitcnt vmcnt(7)
	v_mfma_f32_32x32x16_f16 v[16:31], v[0:3], v[136:139], v[16:31]
	v_pk_add_f16 v0, v7, v6
	s_nop 0
	v_pk_fma_f16 v71, v7, v4, v0 neg_lo:[1,0,0] neg_hi:[1,0,0]
	v_cvt_pk_f16_f32 v0, v8, v9
	v_and_b32_e32 v1, 0x7fff7fff, v0
	v_cvt_pk_f16_f32 v4, v10, v11
	v_pk_fma_f16 v2, v1, s2, v164 op_sel_hi:[1,0,0]
	s_waitcnt vmcnt(6)
	v_mfma_f32_32x32x16_f16 v[16:31], v[64:67], v[140:143], v[16:31]
	v_and_b32_e32 v5, 0x7fff7fff, v4
	v_pk_fma_f16 v2, v2, v1, s3 op_sel_hi:[1,1,0]
	v_pk_fma_f16 v6, v5, s2, v164 op_sel_hi:[1,0,0]
	v_pk_mul_f16 v2, v1, v2
	v_pk_fma_f16 v6, v6, v5, s3 op_sel_hi:[1,1,0]
	v_exp_f16_e32 v3, v2
	v_exp_f16_sdwa v2, v2 dst_sel:DWORD dst_unused:UNUSED_PAD src0_sel:WORD_1
	s_waitcnt vmcnt(5)
	v_mfma_f32_32x32x16_f16 v[16:31], v[72:75], v[144:147], v[16:31]
	v_pk_mul_f16 v6, v5, v6
	v_pk_add_f16 v0, v1, v0
	v_exp_f16_e32 v7, v6
	v_exp_f16_sdwa v6, v6 dst_sel:DWORD dst_unused:UNUSED_PAD src0_sel:WORD_1
	v_pack_b32_f16 v2, v3, v2
	v_pk_fma_f16 v0, v1, v2, v0 neg_lo:[1,0,0] neg_hi:[1,0,0]
	v_pk_add_f16 v2, v5, v4
	s_waitcnt vmcnt(4)
	v_mfma_f32_32x32x16_f16 v[16:31], v[48:51], v[148:151], v[16:31]
	v_pack_b32_f16 v1, v7, v6
	v_pk_fma_f16 v1, v5, v1, v2 neg_lo:[1,0,0] neg_hi:[1,0,0]
	v_cvt_pk_f16_f32 v2, v12, v13
	v_and_b32_e32 v3, 0x7fff7fff, v2
	v_cvt_pk_f16_f32 v6, v14, v15
	v_pk_fma_f16 v4, v3, s2, v164 op_sel_hi:[1,0,0]
	v_and_b32_e32 v7, 0x7fff7fff, v6
	s_waitcnt vmcnt(3)
	v_mfma_f32_32x32x16_f16 v[16:31], v[76:79], v[152:155], v[16:31]
	v_pk_fma_f16 v4, v4, v3, s3 op_sel_hi:[1,1,0]
	v_pk_fma_f16 v8, v7, s2, v164 op_sel_hi:[1,0,0]
	v_pk_mul_f16 v4, v3, v4
	v_pk_fma_f16 v8, v8, v7, s3 op_sel_hi:[1,1,0]
	v_exp_f16_e32 v5, v4
	v_exp_f16_sdwa v4, v4 dst_sel:DWORD dst_unused:UNUSED_PAD src0_sel:WORD_1
	v_pk_mul_f16 v8, v7, v8
	s_waitcnt vmcnt(2)
	v_mfma_f32_32x32x16_f16 v[16:31], v[60:63], v[68:71], v[16:31]
	v_exp_f16_e32 v9, v8
	v_exp_f16_sdwa v8, v8 dst_sel:DWORD dst_unused:UNUSED_PAD src0_sel:WORD_1
	v_pack_b32_f16 v4, v5, v4
	v_pk_add_f16 v2, v3, v2
	s_nop 0
	v_pk_fma_f16 v2, v3, v4, v2 neg_lo:[1,0,0] neg_hi:[1,0,0]
	v_pack_b32_f16 v3, v9, v8
	v_pk_add_f16 v4, v7, v6
	s_nop 0
	v_pk_fma_f16 v3, v7, v3, v4 neg_lo:[1,0,0] neg_hi:[1,0,0]
	global_load_dwordx4 v[4:7], v[56:57], off offset:2048
	s_waitcnt vmcnt(2)
	v_mfma_f32_32x32x16_f16 v[16:31], v[36:39], v[0:3], v[16:31]
	global_load_dwordx4 v[0:3], v[56:57], off offset:1024
	s_waitcnt vmcnt(2)
	v_mfma_f32_32x32x16_f16 v[16:31], v[52:55], v[104:107], v[16:31]
	s_waitcnt vmcnt(0)
	v_mfma_f32_32x32x16_f16 v[16:31], v[0:3], v[100:103], v[16:31]
	global_load_dwordx4 v[0:3], v[56:57], off offset:3072
	v_mfma_f32_32x32x16_f16 v[16:31], v[4:7], v[112:115], v[16:31]
	s_waitcnt vmcnt(0)
	v_mfma_f32_32x32x16_f16 v[16:31], v[0:3], v[108:111], v[16:31]
	s_nop 11
	ds_bpermute_b32 v3, v209, v16
	ds_bpermute_b32 v2, v209, v17
	ds_bpermute_b32 v1, v209, v18
	ds_bpermute_b32 v0, v209, v19
	s_and_saveexec_b64 s[2:3], s[0:1]
	s_cbranch_execz .LBB0_33
	v_max_f32_e32 v4, v17, v17
	v_max_f32_e32 v5, v16, v16
	v_max_f32_e32 v4, v5, v4
	v_max_f32_e32 v5, v19, v19
	v_max_f32_e32 v6, v18, v18
	v_max_f32_e32 v5, v6, v5
	s_waitcnt lgkmcnt(3)
	v_max3_f32 v6, v4, v5, v3
	v_sub_f32_e32 v4, v16, v6
	v_sub_f32_e32 v5, v17, v6
	v_sub_f32_e32 v7, v18, v6
	v_mul_f32_e32 v4, 0x3fb8aa3b, v4
	v_mul_f32_e32 v5, 0x3fb8aa3b, v5
	v_mul_f32_e32 v7, 0x3fb8aa3b, v7
	v_exp_f32_e32 v4, v4
	v_exp_f32_e32 v5, v5
	v_exp_f32_e32 v9, v7
	v_sub_f32_e32 v7, v19, v6
	v_mul_f32_e32 v7, 0x3fb8aa3b, v7
	v_sub_f32_e32 v6, v3, v6
	v_exp_f32_e32 v7, v7
	v_mul_f32_e32 v6, 0x3fb8aa3b, v6
	v_exp_f32_e32 v6, v6
	v_add_f32_e32 v8, v4, v5
	v_add_f32_e32 v8, v9, v8
	v_add_f32_e32 v8, v7, v8
	v_add_f32_e32 v8, v6, v8
	v_rcp_f32_e32 v8, v8
	s_waitcnt lgkmcnt(1)
	v_mul_f32_e32 v1, 0xbfb8aa3b, v1
	v_exp_f32_e32 v1, v1
	s_mov_b32 s1, 0x403fba14
	v_pk_mul_f32 v[6:7], v[6:7], v[8:9] op_sel_hi:[1,0]
	s_mov_b32 s0, 0x40f33a98
	v_pk_mul_f32 v[20:21], v[4:5], v[8:9] op_sel_hi:[1,0]
	v_pk_mul_f32 v[14:15], v[6:7], s[0:1]
	s_mov_b32 s0, 0x411e74af
	v_add_f32_e32 v4, v20, v21
	v_mul_f32_e32 v12, v9, v8
	v_fmac_f32_e32 v4, v9, v8
	v_pk_mul_f32 v[8:9], v[20:21], s[0:1]
	s_mov_b32 s3, 0x4108466c
	s_mov_b32 s2, s1
	v_add_f32_e32 v1, 1.0, v1
	v_mul_f32_e32 v13, 0x411e74af, v6
	v_pk_fma_f32 v[8:9], v[20:21], s[2:3], v[8:9] op_sel:[0,0,1] op_sel_hi:[1,1,0]
	s_mov_b32 s2, 0x40dd0c55
	s_mov_b32 s3, s0
	v_max_f32_e32 v2, v2, v2
	v_rcp_f32_e32 v1, v1
	v_mul_f32_e32 v7, 0x40c6de12, v7
	v_pk_fma_f32 v[8:9], v[12:13], s[2:3], v[8:9] op_sel_hi:[0,1,1]
	v_mov_b32_e32 v6, v15
	v_max_f32_e32 v2, 0xc1400000, v2
	v_pk_add_f32 v[6:7], v[6:7], v[8:9]
	v_mov_b32_e32 v15, v13
	v_min_f32_e32 v2, 0x41400000, v2
	v_pk_add_f32 v[6:7], v[14:15], v[6:7]
	s_mov_b32 s4, 0xbfb8aa3b
	v_mul_f32_e32 v4, v2, v4
	v_sub_f32_e32 v2, v7, v6
	v_fmac_f32_e32 v6, v1, v2
	s_waitcnt lgkmcnt(0)
	v_mul_f32_e64 v1, |v0|, s4
	v_exp_f32_e32 v1, v1
	v_max_f32_e32 v0, v0, v0
	v_mov_b32_e32 v2, 0x411e74af
	v_max_f32_e32 v0, 0, v0
	v_add_f32_e32 v1, 1.0, v1
	v_log_f32_e32 v1, v1
	v_med3_f32 v2, v6, s1, v2
	v_mul_f32_e32 v2, 0x3fb8aa3b, v2
	v_exp_f32_e32 v5, v2
	v_fmamk_f32 v0, v1, 0x3f317218, v0
	v_add_f32_e32 v0, 0x3dcccccd, v0
	v_max_f32_e32 v0, 0x3dcccccd, v0
	v_min_f32_e32 v6, 0x41200000, v0
	v_lshlrev_b32_e32 v0, 3, v158
	v_mov_b32_e32 v10, s38
	v_mov_b32_e32 v11, s39
	v_ashrrev_i32_e32 v1, 31, v0
	v_lshl_add_u64 v[8:9], v[0:1], 2, v[10:11]
	v_mov_b32_e32 v7, v16
	v_pk_mov_b32 v[0:1], v[16:17], v[18:19] op_sel:[1,0]
	v_mov_b32_e32 v2, v19
	global_store_dwordx4 v[8:9], v[4:7], off
	global_store_dwordx4 v[8:9], v[0:3], off offset:16

.Lhead_idle:
	s_barrier
	s_endpgm

_Z19trunk_global_kernelPKfPKDF16_PDF16_S0_S2_S0_S0_PfS4_S0_S0_:
	s_load_dwordx8 s[16:23], s[0:1], 0x0
	s_load_dwordx8 s[8:15], s[0:1], 0x20
	s_lshl_b32 s3, s2, 4
	s_and_b32 s28, s3, 0xffffffe0
	v_lshrrev_b32_e32 v25, 7, v0
	v_lshlrev_b32_e32 v18, 4, v0
	v_or_b32_e32 v1, s28, v25
	v_and_b32_e32 v46, 0x7f0, v18
	v_mov_b32_e32 v47, 0
	v_lshlrev_b32_e32 v2, 9, v1
	s_waitcnt lgkmcnt(0)
	v_lshl_add_u64 v[10:11], s[16:17], 0, v[46:47]
	v_ashrrev_i32_e32 v3, 31, v2
	v_lshl_add_u64 v[12:13], v[2:3], 2, v[10:11]
	v_or_b32_e32 v2, 0x1000, v2
	v_or_b32_e32 v1, s3, v25
	s_and_b32 s30, s2, 1
	v_ashrrev_i32_e32 v3, 31, v2
	v_lshlrev_b32_e32 v1, 9, v1
	v_lshl_add_u64 v[14:15], v[2:3], 2, v[10:11]
	global_load_dwordx4 v[6:9], v[12:13], off nt
	global_load_dwordx4 v[2:5], v[14:15], off nt
	v_or_b32_e32 v12, 0x2000, v1
	s_mul_i32 s3, s30, 0x12980
	v_ashrrev_i32_e32 v13, 31, v12
	s_add_u32 s4, s8, s3
	v_lshrrev_b32_e32 v24, 6, v0
	v_lshl_add_u64 v[20:21], v[12:13], 2, v[10:11]
	v_or_b32_e32 v12, 0x3000, v1
	s_addc_u32 s5, s9, 0
	s_lshl_b32 s3, s2, 3
	v_ashrrev_i32_e32 v13, 31, v12
	v_and_b32_e32 v85, 63, v0
	v_and_or_b32 v82, s3, -16, v24
	v_lshl_add_u64 v[22:23], v[12:13], 2, v[10:11]
	global_load_dwordx4 v[14:17], v[20:21], off nt
	global_load_dwordx4 v[10:13], v[22:23], off nt
	v_lshl_or_b32 v20, v82, 8, v85
	v_ashrrev_i32_e32 v21, 31, v20
	v_lshl_add_u64 v[20:21], v[20:21], 2, s[22:23]
	v_lshlrev_b32_e32 v46, 4, v85
	global_load_dword v81, v[20:21], off
	global_load_dword v80, v[20:21], off offset:256
	global_load_dword v79, v[20:21], off offset:512
	global_load_dword v78, v[20:21], off offset:768
	v_lshl_add_u64 v[20:21], s[4:5], 0, v[46:47]
	s_mov_b32 s3, 0x10000
	s_mov_b64 s[6:7], 0x10980
	v_add_co_u32_e32 v26, vcc, s3, v20
	v_lshl_add_u64 v[22:23], v[20:21], 0, s[6:7]
	s_nop 0
	v_addc_co_u32_e32 v27, vcc, 0, v21, vcc
	s_mov_b32 s3, 0x11000
	global_load_dwordx4 v[74:77], v[22:23], off offset:1024
	global_load_dwordx4 v[70:73], v[22:23], off offset:2048
	global_load_dwordx4 v[34:37], v[26:27], off offset:2432
	global_load_dwordx4 v[62:65], v[22:23], off offset:3072
	v_add_co_u32_e32 v22, vcc, s3, v20
	s_mov_b32 s3, 0x12000
	s_nop 0
	v_addc_co_u32_e32 v23, vcc, 0, v21, vcc
	v_add_co_u32_e32 v20, vcc, s3, v20
	global_load_dwordx4 v[66:69], v[22:23], off offset:2432
	global_load_dwordx4 v[58:61], v[22:23], off offset:3456
	v_addc_co_u32_e32 v21, vcc, 0, v21, vcc
	global_load_dwordx4 v[54:57], v[20:21], off offset:384
	global_load_dwordx4 v[50:53], v[20:21], off offset:1408
	s_load_dwordx2 s[8:9], s[0:1], 0x50
	s_load_dwordx4 s[24:27], s[0:1], 0x40
	v_mov_b32_e32 v19, v47
	s_bitcmp1_b32 s2, 0
	v_lshl_add_u64 v[20:21], s[4:5], 0, v[18:19]
	s_mov_b64 s[0:1], 0x9500
	v_lshlrev_b32_e32 v22, 3, v85
	v_or_b32_e32 v1, 0xfffffc00, v0
	s_cselect_b64 s[6:7], -1, 0
	v_lshl_add_u64 v[20:21], v[20:21], 0, s[0:1]
	s_mov_b64 s[0:1], 0
	s_mov_b64 s[2:3], 0x4000
	s_movk_i32 s16, 0x2ff
	global_load_dwordx4 v[26:29], v[20:21], off
	v_lshl_add_u64 v[20:21], v[20:21], 0, s[2:3]
	v_cmp_gt_u32_e32 vcc, 0x300, v0
	s_nop 1
	s_and_saveexec_b64 s[0:1], vcc
	s_cbranch_execz .Lstage_skip1
	global_load_dwordx4 v[30:33], v[20:21], off
.Lstage_skip1:
	s_or_b64 exec, exec, s[0:1]
	s_waitcnt vmcnt(0)
	ds_write_b128 v18, v[26:29]
	v_add_u32_e32 v18, 0x4000, v18
	s_and_saveexec_b64 s[0:1], vcc
	s_cbranch_execz .Lstage_skip2
	ds_write_b128 v18, v[30:33]
.Lstage_skip2:
	s_or_b64 exec, exec, s[0:1]
	v_mul_u32_u24_e32 v1, 0x1880, v24
	s_movk_i32 s0, 0x7000
	v_mov_b32_e32 v18, 0
	v_or_b32_e32 v23, 0xffffffc0, v85
	v_add3_u32 v26, v1, v46, s0
	s_mov_b64 s[0:1], 0
	v_mov_b32_e32 v19, v18
	v_mov_b32_e32 v20, v18
	v_mov_b32_e32 v21, v18
	s_movk_i32 s2, 0x147
